# NA loop: the two redundant canonicalising v_max x,x,x before the wave-uniform max test removed (the following v_max canonicalises the result), 4 sites, -8 bytes each
# baseline (speedup 1.0000x reference)
.LBB0_1558:
	s_or_b64 exec, exec, s[6:7]
	v_cmp_gt_i32_e32 vcc, 64, v34
	s_and_saveexec_b64 s[6:7], vcc
	v_lshl_add_u32 v1, v34, 2, s43
	ds_write_b32 v1, v149 offset:2400
	s_or_b64 exec, exec, s[6:7]
	s_and_b32 s1, s0, 0x3fffffc0
	s_and_b32 s7, s86, 63
	s_lshl_b32 s1, s1, 2
	s_add_i32 s8, s1, 0
	s_lshl_b32 s1, s7, 2
	v_sub_u32_e64 v1, s1, 4 clamp
	s_ashr_i32 s9, s0, 6
	s_ashr_i32 s0, s0, 7
	v_readfirstlane_b32 s90, v1
	v_sub_u32_e64 v1, s1, 1 clamp
	s_add_i32 s0, s0, s1
	v_readfirstlane_b32 s1, v1
	s_min_u32 s92, s1, 0xf8
	s_max_i32 s10, s0, 4
	s_add_i32 s92, s92, 7
	s_lshl_b32 s16, s11, 7
	s_add_i32 s18, s10, -4
	s_sub_i32 s10, s92, s90
	s_ashr_i32 s17, s16, 31
	s_lshl_b32 s11, s9, 3
	v_bfe_u32 v1, v34, 4, 2
	v_bfe_u32 v2, v34, 2, 3
	v_lshrrev_b32_e32 v3, 1, v34
	s_lshl_b32 s19, s9, 2
	s_add_i32 s8, s8, 0x1e000
	s_lshl_b32 s6, s9, 5
	s_and_b32 s1, s10, -2
	v_bitop3_b32 v2, s11, v176, v2 bitop3:0xc8
	v_and_b32_e32 v3, 8, v3
	s_and_b32 s19, s19, 4
	v_or_b32_e32 v4, s11, v1
	v_bitop3_b32 v1, s11, v34, v1 bitop3:0x36
	s_movk_i32 s11, 0x1800
	s_min_u32 s87, s18, 0xf8
	s_lshl_b64 s[34:35], s[16:17], 1
	v_or3_b32 v2, v3, v2, s19
	v_lshlrev_b32_e32 v3, 3, v34
	v_mul_lo_u32 v5, v4, s11
	v_lshlrev_b32_e32 v1, 3, v1
	s_add_u32 s93, s29, s34
	v_and_b32_e32 v3, 24, v3
	v_mul_u32_u24_e32 v2, 0x1800, v2
	v_and_or_b32 v152, v1, s45, v5
	v_and_b32_e32 v1, 32, v34
	s_addc_u32 s94, s42, s35
	v_or3_b32 v154, v2, v3, v1
	s_add_u32 s38, s5, s34
	v_bitop3_b32 v1, v4, v34, 4 bitop3:0x36
	s_addc_u32 s39, s27, s35
	v_ashrrev_i32_e32 v155, 31, v154
	v_lshlrev_b32_e32 v1, 3, v1
	v_lshl_add_u64 v[2:3], v[154:155], 1, s[38:39]
	s_mov_b64 s[16:17], 0xc000000
	s_lshl_b32 s95, s9, 11
	v_and_or_b32 v1, v1, s45, v5
	v_lshl_add_u64 v[4:5], v[2:3], 0, s[16:17]
	s_mov_b64 s[16:17], 0xc000080
	s_or_b32 s96, s95, 0x400
	s_mov_b32 s9, m0
	s_mov_b32 m0, s95
	s_nop 0
	global_load_lds_dwordx4 v[4:5], off
	s_mov_b32 m0, s9
	v_lshl_add_u64 v[4:5], v[2:3], 0, s[16:17]
	s_add_u32 s16, s93, 0xc000000
	v_ashrrev_i32_e32 v153, 31, v152
	v_add_u32_e32 v156, 0x6000, v1
	s_mov_b32 s9, m0
	s_mov_b32 m0, s96
	s_nop 0
	global_load_lds_dwordx4 v[4:5], off
	s_mov_b32 m0, s9
	s_addc_u32 s17, s94, 0
	v_lshlrev_b64 v[4:5], 1, v[152:153]
	v_lshl_add_u64 v[6:7], s[16:17], 0, v[4:5]
	s_add_i32 s9, s95, 0x4000
	v_ashrrev_i32_e32 v157, 31, v156
	s_mov_b32 s11, m0
	s_mov_b32 m0, s9
	s_nop 0
	global_load_lds_dwordx4 v[6:7], off
	s_mov_b32 m0, s11
	v_lshlrev_b64 v[6:7], 1, v[156:157]
	s_add_i32 s9, s95, 0x4400
	v_lshl_add_u64 v[8:9], s[16:17], 0, v[6:7]
	s_mov_b32 s11, m0
	s_mov_b32 m0, s9
	s_nop 0
	global_load_lds_dwordx4 v[8:9], off
	s_mov_b32 m0, s11
	s_mov_b64 s[16:17], 0xc0c0000
	s_add_i32 s9, s95, 0x8000
	v_lshl_add_u64 v[8:9], v[2:3], 0, s[16:17]
	s_mov_b32 s11, m0
	s_mov_b32 m0, s9
	s_nop 0
	global_load_lds_dwordx4 v[8:9], off
	s_mov_b32 m0, s11
	s_mov_b64 s[16:17], 0xc0c0080
	s_add_i32 s9, s95, 0x8400
	v_lshl_add_u64 v[2:3], v[2:3], 0, s[16:17]
	s_add_u32 s16, s93, 0xc0c0000
	s_addc_u32 s17, s94, 0
	s_mov_b32 s11, m0
	s_mov_b32 m0, s9
	s_nop 0
	global_load_lds_dwordx4 v[2:3], off
	s_mov_b32 m0, s11
	v_lshl_add_u64 v[2:3], s[16:17], 0, v[4:5]
	s_lshl_b32 s7, s7, 8
	v_and_b32_e32 v179, 31, v34
	s_add_i32 s9, s95, 0xc000
	s_mov_b32 s11, m0
	s_mov_b32 m0, s9
	s_nop 0
	global_load_lds_dwordx4 v[2:3], off
	s_mov_b32 m0, s11
	v_lshl_add_u64 v[2:3], s[16:17], 0, v[6:7]
	s_add_i32 s36, s6, s7
	s_add_i32 s9, s95, 0xc400
	s_mov_b32 s11, m0
	s_mov_b32 m0, s9
	s_nop 0
	global_load_lds_dwordx4 v[2:3], off
	s_mov_b32 m0, s11
	v_or_b32_e32 v1, s36, v179
	v_mov_b64_e32 v[2:3], s[24:25]
	v_bfe_u32 v178, v34, 5, 1
	v_mad_i64_i32 v[2:3], s[16:17], v1, s46, v[2:3]
	v_lshl_add_u64 v[2:3], v[2:3], 0, s[34:35]
	v_lshlrev_b32_e32 v148, 4, v178
	v_lshl_add_u64 v[2:3], v[2:3], 0, v[148:149]
	global_load_dwordx4 v[136:139], v[2:3], off
	global_load_dwordx4 v[132:135], v[2:3], off offset:32
	global_load_dwordx4 v[128:131], v[2:3], off offset:64
	global_load_dwordx4 v[124:127], v[2:3], off offset:96
	global_load_dwordx4 v[120:123], v[2:3], off offset:128
	global_load_dwordx4 v[116:119], v[2:3], off offset:160
	global_load_dwordx4 v[112:115], v[2:3], off offset:192
	global_load_dwordx4 v[108:111], v[2:3], off offset:224
	v_lshlrev_b32_e32 v35, 4, v34
	v_lshlrev_b32_e32 v191, 8, v179
	s_movk_i32 s7, 0xf0
	v_add_u32_e32 v194, 0, v191
	v_bitop3_b32 v192, v148, v35, s7 bitop3:0x78
	s_waitcnt vmcnt(8) lgkmcnt(0)
	s_barrier
	v_add_u32_e32 v1, v194, v192
	ds_read_b128 v[2:5], v1 offset:16384
	ds_read_b128 v[6:9], v1 offset:24576
	s_waitcnt vmcnt(7) lgkmcnt(1)
	v_mfma_f32_32x32x16_bf16 v[18:33], v[2:5], v[136:139], 0
	v_and_b32_e32 v44, 0xf0, v35
	v_bitop3_b32 v193, v148, v44, 32 bitop3:0x36
	v_add_u32_e32 v1, v194, v193
	ds_read_b128 v[36:39], v1 offset:16384
	ds_read_b128 v[40:43], v1 offset:24576
	v_bitop3_b32 v187, v148, v44, 64 bitop3:0x36
	v_add_u32_e32 v1, v194, v187
	s_movk_i32 s7, 0x60
	s_waitcnt lgkmcnt(2)
	v_mfma_f32_32x32x16_bf16 v[2:17], v[6:9], v[136:139], 0
	v_bitop3_b32 v186, v148, v44, s7 bitop3:0x36
	s_movk_i32 s7, 0x80
	v_bitop3_b32 v189, v148, v44, s7 bitop3:0x36
	s_movk_i32 s7, 0xa0
	v_bitop3_b32 v190, v148, v44, s7 bitop3:0x36
	s_movk_i32 s7, 0xc0
	v_bitop3_b32 v185, v148, v44, s7 bitop3:0x36
	s_waitcnt vmcnt(6) lgkmcnt(1)
	v_mfma_f32_32x32x16_bf16 v[18:33], v[36:39], v[132:135], v[18:33]
	v_and_or_b32 v45, s6, 32, v179
	s_movk_i32 s6, 0xe0
	v_bitop3_b32 v188, v148, v44, s6 bitop3:0x36
	v_add_u32_e32 v44, v194, v188
	s_mov_b64 s[6:7], 0xffff
	v_and_b32_e32 v180, 63, v34
	v_and_b32_e32 v35, 0xc0, v35
	s_waitcnt lgkmcnt(0)
	v_mfma_f32_32x32x16_bf16 v[2:17], v[40:43], v[132:135], v[2:17]
	ds_read_b128 v[36:39], v1 offset:16384
	ds_read_b128 v[40:43], v1 offset:24576
	v_add_u32_e32 v1, v194, v186
	v_lshlrev_b32_e32 v34, 1, v34
	v_and_b32_e32 v34, 32, v34
	s_mov_b32 s89, 0x8000
	s_mov_b32 s91, 0
	s_add_i32 s88, s87, 8
	s_waitcnt vmcnt(5) lgkmcnt(1)
	v_mfma_f32_32x32x16_bf16 v[18:33], v[36:39], v[128:131], v[18:33]
	s_waitcnt lgkmcnt(0)
	v_mfma_f32_32x32x16_bf16 v[2:17], v[40:43], v[128:131], v[2:17]
	ds_read_b128 v[36:39], v1 offset:16384
	ds_read_b128 v[40:43], v1 offset:24576
	v_add_u32_e32 v1, v194, v189
	s_waitcnt vmcnt(4) lgkmcnt(1)
	v_mfma_f32_32x32x16_bf16 v[18:33], v[36:39], v[124:127], v[18:33]
	s_waitcnt lgkmcnt(0)
	v_mfma_f32_32x32x16_bf16 v[2:17], v[40:43], v[124:127], v[2:17]
	ds_read_b128 v[36:39], v1 offset:16384
	ds_read_b128 v[40:43], v1 offset:24576
	v_add_u32_e32 v1, v194, v190
	s_waitcnt vmcnt(3) lgkmcnt(1)
	v_mfma_f32_32x32x16_bf16 v[18:33], v[36:39], v[120:123], v[18:33]
	s_waitcnt lgkmcnt(0)
	v_mfma_f32_32x32x16_bf16 v[2:17], v[40:43], v[120:123], v[2:17]
	ds_read_b128 v[36:39], v1 offset:16384
	ds_read_b128 v[40:43], v1 offset:24576
	v_add_u32_e32 v1, v194, v185
	s_waitcnt vmcnt(2) lgkmcnt(1)
	v_mfma_f32_32x32x16_bf16 v[18:33], v[36:39], v[116:119], v[18:33]
	ds_read_b128 v[36:39], v1 offset:16384
	s_waitcnt lgkmcnt(1)
	v_mfma_f32_32x32x16_bf16 v[2:17], v[40:43], v[116:119], v[2:17]
	ds_read_b128 v[40:43], v1 offset:24576
	v_sub_u32_e64 v1, v45, 8 clamp
	v_min_u32_e32 v46, 48, v1
	v_lshlrev_b32_e32 v1, 2, v178
	v_sub_u32_e32 v183, v1, v45
	v_lshlrev_b32_e32 v45, 3, v180
	v_and_or_b32 v35, v45, 24, v35
	s_waitcnt vmcnt(1) lgkmcnt(1)
	v_mfma_f32_32x32x16_bf16 v[18:33], v[36:39], v[112:115], v[18:33]
	ds_read_b128 v[36:39], v44 offset:16384
	s_waitcnt lgkmcnt(1)
	v_mfma_f32_32x32x16_bf16 v[2:17], v[40:43], v[112:115], v[2:17]
	v_lshlrev_b64 v[40:41], v46, s[6:7]
	v_lshrrev_b64 v[150:151], v1, v[40:41]
	v_lshrrev_b32_e32 v184, v1, v41
	ds_read_b128 v[40:43], v44 offset:24576
	s_waitcnt vmcnt(0) lgkmcnt(1)
	v_mfma_f32_32x32x16_bf16 v[18:33], v[36:39], v[108:111], v[18:33]
	v_and_b32_e32 v36, 0x100, v45
	v_or3_b32 v148, v35, v34, v36
	v_mov_b32_e32 v34, s47
	v_mov_b32_e32 v35, s48
	v_mov_b32_e32 v36, s49
	v_mov_b32_e32 v37, s50
	v_mov_b32_e32 v38, s51
	s_waitcnt lgkmcnt(0)
	v_mfma_f32_32x32x16_bf16 v[2:17], v[40:43], v[108:111], v[2:17]
	v_mov_b32_e32 v39, s52
	v_mov_b32_e32 v40, s53
	v_mov_b32_e32 v41, s54
	ds_read_b32 v34, v34
	ds_read_b32 v35, v35
	ds_read_b32 v36, v36
	ds_read_b32 v37, v37
	ds_read_b32 v38, v38
	ds_read_b32 v39, v39
	ds_read_b32 v40, v40
	ds_read_b32 v41, v41
	s_waitcnt lgkmcnt(7)
	v_bfi_b32 v34, v174, v34, v175
	s_waitcnt lgkmcnt(6)
	v_bfi_b32 v35, v174, v35, v175
	s_nop 0
	v_pk_fma_f32 v[18:19], v[18:19], s[28:29], v[34:35] op_sel_hi:[1,0,1]
	s_waitcnt lgkmcnt(5)
	v_bfi_b32 v34, v174, v36, v175
	s_waitcnt lgkmcnt(4)
	v_bfi_b32 v35, v174, v37, v175
	s_nop 0
	v_pk_fma_f32 v[20:21], v[20:21], s[28:29], v[34:35] op_sel_hi:[1,0,1]
	s_waitcnt lgkmcnt(3)
	v_bfi_b32 v34, v174, v38, v175
	s_waitcnt lgkmcnt(2)
	v_bfi_b32 v35, v174, v39, v175
	s_nop 0
	v_pk_fma_f32 v[22:23], v[22:23], s[28:29], v[34:35] op_sel_hi:[1,0,1]
	s_waitcnt lgkmcnt(1)
	v_bfi_b32 v34, v174, v40, v175
	s_waitcnt lgkmcnt(0)
	v_bfi_b32 v35, v174, v41, v175
	s_nop 0
	v_pk_fma_f32 v[24:25], v[24:25], s[28:29], v[34:35] op_sel_hi:[1,0,1]
	v_mov_b32_e32 v34, s55
	v_mov_b32_e32 v35, s56
	v_mov_b32_e32 v36, s57
	v_mov_b32_e32 v37, s58
	v_mov_b32_e32 v38, s59
	v_mov_b32_e32 v39, s61
	v_mov_b32_e32 v40, s66
	v_mov_b32_e32 v41, s67
	ds_read_b32 v34, v34
	ds_read_b32 v35, v35
	ds_read_b32 v36, v36
	ds_read_b32 v37, v37
	ds_read_b32 v38, v38
	ds_read_b32 v39, v39
	ds_read_b32 v40, v40
	ds_read_b32 v41, v41
	s_waitcnt lgkmcnt(7)
	v_bfi_b32 v34, v174, v34, v175
	s_waitcnt lgkmcnt(6)
	v_bfi_b32 v35, v174, v35, v175
	s_nop 0
	v_pk_fma_f32 v[26:27], v[26:27], s[28:29], v[34:35] op_sel_hi:[1,0,1]
	s_waitcnt lgkmcnt(5)
	v_bfi_b32 v34, v174, v36, v175
	s_waitcnt lgkmcnt(4)
	v_bfi_b32 v35, v174, v37, v175
	s_nop 0
	v_pk_fma_f32 v[28:29], v[28:29], s[28:29], v[34:35] op_sel_hi:[1,0,1]
	s_waitcnt lgkmcnt(3)
	v_bfi_b32 v34, v174, v38, v175
	s_waitcnt lgkmcnt(2)
	v_bfi_b32 v35, v174, v39, v175
	s_nop 0
	v_pk_fma_f32 v[30:31], v[30:31], s[28:29], v[34:35] op_sel_hi:[1,0,1]
	s_waitcnt lgkmcnt(1)
	v_bfi_b32 v34, v174, v40, v175
	s_waitcnt lgkmcnt(0)
	v_bfi_b32 v35, v174, v41, v175
	s_nop 0
	v_pk_fma_f32 v[32:33], v[32:33], s[28:29], v[34:35] op_sel_hi:[1,0,1]
	v_mov_b32_e32 v34, s68
	v_mov_b32_e32 v35, s69
	v_mov_b32_e32 v36, s70
	v_mov_b32_e32 v37, s71
	v_mov_b32_e32 v38, s72
	v_mov_b32_e32 v39, s73
	v_mov_b32_e32 v40, s74
	v_mov_b32_e32 v41, s75
	ds_read_b32 v34, v34
	ds_read_b32 v35, v35
	ds_read_b32 v36, v36
	ds_read_b32 v37, v37
	ds_read_b32 v38, v38
	ds_read_b32 v39, v39
	ds_read_b32 v40, v40
	ds_read_b32 v41, v41
	s_waitcnt lgkmcnt(7)
	v_bfi_b32 v34, v174, v34, v175
	s_waitcnt lgkmcnt(6)
	v_bfi_b32 v35, v174, v35, v175
	s_nop 0
	v_pk_fma_f32 v[2:3], v[2:3], s[28:29], v[34:35] op_sel_hi:[1,0,1]
	s_waitcnt lgkmcnt(5)
	v_bfi_b32 v34, v174, v36, v175
	s_waitcnt lgkmcnt(4)
	v_bfi_b32 v35, v174, v37, v175
	s_nop 0
	v_pk_fma_f32 v[4:5], v[4:5], s[28:29], v[34:35] op_sel_hi:[1,0,1]
	s_waitcnt lgkmcnt(3)
	v_bfi_b32 v34, v174, v38, v175
	s_waitcnt lgkmcnt(2)
	v_bfi_b32 v35, v174, v39, v175
	s_nop 0
	v_pk_fma_f32 v[6:7], v[6:7], s[28:29], v[34:35] op_sel_hi:[1,0,1]
	s_waitcnt lgkmcnt(1)
	v_bfi_b32 v34, v174, v40, v175
	s_waitcnt lgkmcnt(0)
	v_bfi_b32 v35, v174, v41, v175
	s_nop 0
	v_pk_fma_f32 v[8:9], v[8:9], s[28:29], v[34:35] op_sel_hi:[1,0,1]
	v_mov_b32_e32 v34, s76
	v_mov_b32_e32 v35, s77
	v_mov_b32_e32 v36, s78
	v_mov_b32_e32 v37, s79
	v_mov_b32_e32 v38, s80
	v_mov_b32_e32 v39, s81
	v_mov_b32_e32 v40, s82
	v_mov_b32_e32 v41, s83
	ds_read_b32 v34, v34
	ds_read_b32 v35, v35
	ds_read_b32 v36, v36
	ds_read_b32 v37, v37
	ds_read_b32 v38, v38
	ds_read_b32 v39, v39
	ds_read_b32 v40, v40
	ds_read_b32 v41, v41
	s_waitcnt lgkmcnt(7)
	v_bfi_b32 v34, v174, v34, v175
	s_waitcnt lgkmcnt(6)
	v_bfi_b32 v35, v174, v35, v175
	s_nop 0
	v_pk_fma_f32 v[10:11], v[10:11], s[28:29], v[34:35] op_sel_hi:[1,0,1]
	s_waitcnt lgkmcnt(5)
	v_bfi_b32 v34, v174, v36, v175
	s_waitcnt lgkmcnt(4)
	v_bfi_b32 v35, v174, v37, v175
	s_nop 0
	v_pk_fma_f32 v[12:13], v[12:13], s[28:29], v[34:35] op_sel_hi:[1,0,1]
	s_waitcnt lgkmcnt(3)
	v_bfi_b32 v34, v174, v38, v175
	s_waitcnt lgkmcnt(2)
	v_bfi_b32 v35, v174, v39, v175
	s_nop 0
	v_pk_fma_f32 v[14:15], v[14:15], s[28:29], v[34:35] op_sel_hi:[1,0,1]
	s_waitcnt lgkmcnt(1)
	v_bfi_b32 v34, v174, v40, v175
	s_waitcnt lgkmcnt(0)
	v_bfi_b32 v35, v174, v41, v175
	s_nop 0
	v_pk_fma_f32 v[16:17], v[16:17], s[28:29], v[34:35] op_sel_hi:[1,0,1]
	v_max_f32_e32 v34, v18, v19
	v_max3_f32 v34, v34, v20, v21
	v_max3_f32 v34, v34, v22, v23
	v_max3_f32 v34, v34, v24, v25
	v_max3_f32 v34, v34, v26, v27
	v_max3_f32 v34, v34, v28, v29
	v_max3_f32 v34, v34, v30, v31
	v_max3_f32 v34, v34, v32, v33
	v_max3_f32 v34, v34, v2, v3
	v_max3_f32 v34, v34, v4, v5
	v_max3_f32 v34, v34, v6, v7
	v_max3_f32 v34, v34, v8, v9
	v_max3_f32 v34, v34, v10, v11
	v_max3_f32 v34, v34, v12, v13
	v_max3_f32 v34, v34, v14, v15
	v_max3_f32 v34, v34, v16, v17
	v_mov_b32_e32 v35, v34
	s_nop 1
	v_permlane32_swap_b32_e32 v34, v35
	v_max_f32_e32 v34, v34, v35
	v_add_f32_e32 v35, 0x7149f2ca, v34
	v_cmp_ge_f32_e32 vcc, s84, v35
	s_cmp_eq_u64 vcc, exec
	v_max_f32_e32 v34, 0xf149f2ca, v34
	s_cselect_b64 vcc, -1, 0
	v_sub_f32_e32 v35, 0xf149f2ca, v34
	v_cndmask_b32_e32 v198, v34, v177, vcc
	v_exp_f32_e32 v35, v35
	v_sub_f32_e32 v33, v33, v198
	v_sub_f32_e32 v32, v32, v198
	v_sub_f32_e32 v31, v31, v198
	v_sub_f32_e32 v30, v30, v198
	v_sub_f32_e32 v29, v29, v198
	v_sub_f32_e32 v28, v28, v198
	v_sub_f32_e32 v27, v27, v198
	v_sub_f32_e32 v26, v26, v198
	v_sub_f32_e32 v25, v25, v198
	v_sub_f32_e32 v24, v24, v198
	v_sub_f32_e32 v23, v23, v198
	v_sub_f32_e32 v22, v22, v198
	v_sub_f32_e32 v21, v21, v198
	v_sub_f32_e32 v20, v20, v198
	v_sub_f32_e32 v19, v19, v198
	v_sub_f32_e32 v18, v18, v198
	v_exp_f32_e32 v166, v18
	v_exp_f32_e32 v167, v19
	v_exp_f32_e32 v164, v20
	v_exp_f32_e32 v165, v21
	v_exp_f32_e32 v162, v22
	v_exp_f32_e32 v163, v23
	v_exp_f32_e32 v160, v24
	v_exp_f32_e32 v161, v25
	v_exp_f32_e32 v146, v26
	v_exp_f32_e32 v147, v27
	v_exp_f32_e32 v144, v28
	v_exp_f32_e32 v145, v29
	v_exp_f32_e32 v142, v30
	v_exp_f32_e32 v143, v31
	v_exp_f32_e32 v140, v32
	v_exp_f32_e32 v141, v33
	s_add_i32 s97, s1, 5
	v_cndmask_b32_e64 v195, v35, 1.0, vcc
	v_sub_f32_e32 v67, v17, v198
	v_sub_f32_e32 v66, v16, v198
	v_sub_f32_e32 v69, v15, v198
	v_sub_f32_e32 v68, v14, v198
	v_sub_f32_e32 v71, v13, v198
	s_cmp_lt_i32 s1, -3
	v_cmp_gt_u32_e64 s[6:7], 32, v180
	v_lshl_add_u32 v181, v179, 2, s8
	v_lshl_add_u32 v151, v1, 2, s8
	v_sub_f32_e32 v70, v12, v198
	v_sub_f32_e32 v73, v11, v198
	v_sub_f32_e32 v72, v10, v198
	v_sub_f32_e32 v75, v9, v198
	v_sub_f32_e32 v74, v8, v198
	v_sub_f32_e32 v77, v7, v198
	v_sub_f32_e32 v76, v6, v198
	v_sub_f32_e32 v79, v5, v198
	v_sub_f32_e32 v78, v4, v198
	v_sub_f32_e32 v1, v3, v198
	v_sub_f32_e32 v80, v2, v198
	v_mov_b32_e32 v17, 0
	s_cbranch_scc1 .LBB0_1586
	s_and_b32 s8, s85, 63
	s_lshl_b32 s8, s8, 2
	s_min_u32 s9, s8, 4
	v_mov_b32_e32 v182, 0
	s_add_i32 s37, s10, 4
	s_add_i32 s44, s10, 3
	s_sub_i32 s11, s8, s9
	s_mov_b32 s33, 2
	v_lshl_add_u32 v196, v183, 2, s43
	s_mov_b32 s64, 1
	s_mov_b32 s8, 0
	s_movk_i32 s65, 0x4080
	s_mov_b32 s16, 1
	v_mov_b32_e32 v50, 0
	v_mov_b32_e32 v51, v182
	v_mov_b32_e32 v52, v182
	v_mov_b32_e32 v53, v182
	v_mov_b32_e32 v54, v182
	v_mov_b32_e32 v55, v182
	v_mov_b32_e32 v56, v182
	v_mov_b32_e32 v57, v182
	v_mov_b32_e32 v58, v182
	v_mov_b32_e32 v59, v182
	v_mov_b32_e32 v60, v182
	v_mov_b32_e32 v61, v182
	v_mov_b32_e32 v62, v182
	v_mov_b32_e32 v63, v182
	v_mov_b32_e32 v64, v182
	v_mov_b32_e32 v65, v182
	v_mov_b32_e32 v34, 0
	v_mov_b32_e32 v35, v182
	v_mov_b32_e32 v36, v182
	v_mov_b32_e32 v37, v182
	v_mov_b32_e32 v38, v182
	v_mov_b32_e32 v39, v182
	v_mov_b32_e32 v40, v182
	v_mov_b32_e32 v41, v182
	v_mov_b32_e32 v42, v182
	v_mov_b32_e32 v43, v182
	v_mov_b32_e32 v44, v182
	v_mov_b32_e32 v45, v182
	v_mov_b32_e32 v46, v182
	v_mov_b32_e32 v47, v182
	v_mov_b32_e32 v48, v182
	v_mov_b32_e32 v49, v182
	v_mov_b32_e32 v18, 0
	v_mov_b32_e32 v19, v182
	v_mov_b32_e32 v20, v182
	v_mov_b32_e32 v21, v182
	v_mov_b32_e32 v22, v182
	v_mov_b32_e32 v23, v182
	v_mov_b32_e32 v24, v182
	v_mov_b32_e32 v25, v182
	v_mov_b32_e32 v26, v182
	v_mov_b32_e32 v27, v182
	v_mov_b32_e32 v28, v182
	v_mov_b32_e32 v29, v182
	v_mov_b32_e32 v30, v182
	v_mov_b32_e32 v31, v182
	v_mov_b32_e32 v32, v182
	v_mov_b32_e32 v33, v182
	v_mov_b32_e32 v2, 0
	v_mov_b32_e32 v3, v182
	v_mov_b32_e32 v4, v182
	v_mov_b32_e32 v5, v182
	v_mov_b32_e32 v6, v182
	v_mov_b32_e32 v7, v182
	v_mov_b32_e32 v8, v182
	v_mov_b32_e32 v9, v182
	v_mov_b32_e32 v10, v182
	v_mov_b32_e32 v11, v182
	v_mov_b32_e32 v12, v182
	v_mov_b32_e32 v13, v182
	v_mov_b32_e32 v14, v182
	v_mov_b32_e32 v15, v182
	v_mov_b32_e32 v16, v182
	v_mov_b32_e32 v17, v182

.LBB0_1566:
	s_lshl_b32 s91, s33, 15
	s_mul_hi_i32 s20, s19, 0x3000
	s_mulk_i32 s19, 0x3000
	s_add_u32 s8, s38, s19
	s_addc_u32 s9, s39, s20
	v_lshl_add_u64 v[82:83], v[154:155], 1, s[8:9]
	s_add_i32 s8, s91, s95
	s_mov_b32 s9, m0
	s_mov_b32 m0, s8
	s_nop 0
	global_load_lds_dwordx4 v[82:83], off
	s_mov_b32 m0, s9
	s_add_i32 s8, s91, s96
	v_lshl_add_u64 v[82:83], v[82:83], 0, s[30:31]
	s_mov_b32 s9, m0
	s_mov_b32 m0, s8
	s_nop 0
	global_load_lds_dwordx4 v[82:83], off
	s_mov_b32 m0, s9
	s_add_u32 s8, s93, s19
	s_addc_u32 s9, s94, s20
	s_or_b32 s19, s91, 0x4000
	v_lshl_add_u64 v[82:83], v[152:153], 1, s[8:9]
	s_add_i32 s20, s19, s95
	s_mov_b32 s21, m0
	s_mov_b32 m0, s20
	s_nop 0
	global_load_lds_dwordx4 v[82:83], off
	s_mov_b32 m0, s21
	v_lshl_add_u64 v[82:83], v[156:157], 1, s[8:9]
	s_add_i32 s19, s19, s96
	s_mov_b32 s8, m0
	s_mov_b32 m0, s19
	s_nop 0
	global_load_lds_dwordx4 v[82:83], off
	s_mov_b32 m0, s8
	s_lshl_b32 s19, s17, 15
	v_exp_f32_e32 v173, v1
	v_add_u32_e32 v1, s19, v194
	v_add_u32_e32 v82, v1, v192
	v_exp_f32_e32 v172, v80
	v_exp_f32_e32 v168, v78
	v_exp_f32_e32 v169, v79
	ds_read_b128 v[78:81], v82 offset:16384
	v_add_u32_e32 v158, v1, v193
	v_exp_f32_e32 v170, v76
	v_exp_f32_e32 v171, v77
	ds_read_b128 v[200:203], v158 offset:24576
	s_waitcnt lgkmcnt(1)
	v_mfma_f32_32x32x16_bf16 v[92:107], v[78:81], v[136:139], 0
	ds_read_b128 v[76:79], v158 offset:16384
	v_add_u32_e32 v158, v1, v187
	v_exp_f32_e32 v236, v72
	v_add_u32_e32 v72, v1, v185
	v_exp_f32_e32 v74, v74
	v_exp_f32_e32 v75, v75
	v_exp_f32_e32 v237, v73
	s_waitcnt lgkmcnt(0)
	v_mfma_f32_32x32x16_bf16 v[92:107], v[76:79], v[132:135], v[92:107]
	ds_read_b128 v[76:79], v82 offset:24576
	v_exp_f32_e32 v238, v70
	v_exp_f32_e32 v239, v71
	s_waitcnt lgkmcnt(0)
	v_mfma_f32_32x32x16_bf16 v[76:91], v[76:79], v[136:139], 0
	v_mfma_f32_32x32x16_bf16 v[76:91], v[200:203], v[132:135], v[76:91]
	ds_read_b128 v[200:203], v158 offset:16384
	s_waitcnt lgkmcnt(0)
	v_mfma_f32_32x32x16_bf16 v[92:107], v[200:203], v[128:131], v[92:107]
	ds_read_b128 v[200:203], v158 offset:24576
	v_add_u32_e32 v158, v1, v186
	ds_read_b128 v[204:207], v158 offset:16384
	ds_read_b128 v[208:211], v158 offset:24576
	v_add_u32_e32 v158, v1, v189
	s_waitcnt lgkmcnt(2)
	v_mfma_f32_32x32x16_bf16 v[76:91], v[200:203], v[128:131], v[76:91]
	ds_read_b128 v[200:203], v158 offset:16384
	ds_read_b128 v[212:215], v158 offset:24576
	v_add_u32_e32 v158, v1, v190
	ds_read_b128 v[216:219], v158 offset:16384
	ds_read_b128 v[220:223], v158 offset:24576
	v_add_u32_e32 v1, v1, v188
	s_waitcnt lgkmcnt(5)
	v_mfma_f32_32x32x16_bf16 v[92:107], v[204:207], v[124:127], v[92:107]
	ds_read_b128 v[204:207], v72 offset:16384
	ds_read_b128 v[224:227], v72 offset:24576
	ds_read_b128 v[228:231], v1 offset:16384
	ds_read_b128 v[232:235], v1 offset:24576
	s_waitcnt lgkmcnt(8)
	v_mfma_f32_32x32x16_bf16 v[76:91], v[208:211], v[124:127], v[76:91]
	v_exp_f32_e32 v210, v66
	v_exp_f32_e32 v211, v67
	v_pk_add_f32 v[66:67], v[166:167], 0 op_sel_hi:[1,0]
	v_exp_f32_e32 v208, v68
	v_pk_add_f32 v[66:67], v[66:67], v[172:173]
	v_exp_f32_e32 v209, v69
	v_pk_add_f32 v[66:67], v[164:165], v[66:67]
	s_waitcnt lgkmcnt(7)
	v_mfma_f32_32x32x16_bf16 v[92:107], v[200:203], v[120:123], v[92:107]
	v_add_f32_e64 v66, v168, v66
	v_add_f32_e64 v67, v169, v67
	v_add_f32_e64 v66, v162, v66
	v_add_f32_e64 v67, v163, v67
	v_add_f32_e64 v66, v170, v66
	v_add_f32_e64 v67, v171, v67
	v_pk_add_f32 v[66:67], v[160:161], v[66:67]
	s_waitcnt lgkmcnt(6)
	v_mfma_f32_32x32x16_bf16 v[76:91], v[212:215], v[120:123], v[76:91]
	v_add_f32_e64 v66, v74, v66
	v_add_f32_e64 v67, v75, v67
	v_add_f32_e64 v66, v146, v66
	v_add_f32_e64 v67, v147, v67
	v_add_f32_e64 v66, v236, v66
	v_add_f32_e64 v67, v237, v67
	v_pk_add_f32 v[66:67], v[144:145], v[66:67]
	s_waitcnt lgkmcnt(5)
	v_mfma_f32_32x32x16_bf16 v[92:107], v[216:219], v[116:119], v[92:107]
	v_add_f32_e64 v66, v238, v66
	v_add_f32_e64 v67, v239, v67
	v_add_f32_e64 v66, v142, v66
	v_add_f32_e64 v67, v143, v67
	v_add_f32_e64 v66, v208, v66
	v_add_f32_e64 v67, v209, v67
	v_pk_add_f32 v[66:67], v[140:141], v[66:67]
	s_waitcnt lgkmcnt(4)
	v_mfma_f32_32x32x16_bf16 v[76:91], v[220:223], v[116:119], v[76:91]
	v_add_f32_e64 v66, v210, v66
	v_add_f32_e64 v67, v211, v67
	v_add_f32_e64 v158, v66, v67
	v_add_f32_e64 v159, v67, v66
	v_cvt_pk_bf16_f32 v66, v166, v167
	v_cvt_pk_bf16_f32 v67, v164, v165
	v_cvt_pk_bf16_f32 v68, v162, v163
	v_cvt_pk_bf16_f32 v69, v160, v161
	s_waitcnt lgkmcnt(3)
	v_mfma_f32_32x32x16_bf16 v[92:107], v[204:207], v[112:115], v[92:107]
	v_mov_b32_e32 v197, v158
	v_cvt_pk_bf16_f32 v70, v146, v147
	v_cvt_pk_bf16_f32 v71, v144, v145
	v_cvt_pk_bf16_f32 v72, v142, v143
	v_cvt_pk_bf16_f32 v73, v140, v141
	s_nop 1
	v_permlane32_swap_b32_e32 v158, v197
	s_waitcnt lgkmcnt(2)
	v_mfma_f32_32x32x16_bf16 v[76:91], v[224:227], v[112:115], v[76:91]
	v_permlane32_swap_b32_e32 v66, v68
	v_permlane32_swap_b32_e32 v67, v69
	v_permlane32_swap_b32_e32 v70, v72
	v_permlane32_swap_b32_e32 v71, v73
	s_waitcnt lgkmcnt(1)
	v_mfma_f32_32x32x16_bf16 v[92:107], v[228:231], v[108:111], v[92:107]
	v_cvt_pk_bf16_f32 v140, v172, v173
	v_cvt_pk_bf16_f32 v141, v168, v169
	v_cvt_pk_bf16_f32 v142, v170, v171
	v_cvt_pk_bf16_f32 v143, v74, v75
	v_cvt_pk_bf16_f32 v144, v236, v237
	v_cvt_pk_bf16_f32 v145, v238, v239
	v_cvt_pk_bf16_f32 v146, v208, v209
	s_waitcnt lgkmcnt(0)
	v_mfma_f32_32x32x16_bf16 v[76:91], v[232:235], v[108:111], v[76:91]
	v_cvt_pk_bf16_f32 v147, v210, v211
	v_permlane32_swap_b32_e32 v140, v142
	v_permlane32_swap_b32_e32 v141, v143
	v_permlane32_swap_b32_e32 v144, v146
	v_permlane32_swap_b32_e32 v145, v147
	s_lshl_b32 s89, s64, 15
	v_or_b32_e32 v1, s89, v148
	ds_read_b64_tr_b16 v[160:161], v1
	ds_read_b64_tr_b16 v[162:163], v1 offset:2048
	ds_read_b64_tr_b16 v[164:165], v1 offset:4096
	ds_read_b64_tr_b16 v[166:167], v1 offset:6144
	ds_read_b64_tr_b16 v[168:169], v1 offset:8192
	ds_read_b64_tr_b16 v[170:171], v1 offset:10240
	ds_read_b64_tr_b16 v[200:201], v1 offset:12288
	ds_read_b64_tr_b16 v[202:203], v1 offset:14336
	s_waitcnt lgkmcnt(6)
	v_mfma_f32_32x32x16_bf16 v[50:65], v[66:69], v[160:163], v[50:65]
	s_add_i32 s8, s18, -4
	s_cmp_le_i32 s16, s37
	s_cselect_b32 s8, s8, 0xfffffc18
	s_cmp_gt_u32 s16, 3
	s_cselect_b32 s62, s8, -1
	s_cmp_lg_u32 s62, -1
	s_cselect_b64 vcc, -1, 0
	s_waitcnt lgkmcnt(4)
	v_mfma_f32_32x32x16_bf16 v[50:65], v[70:73], v[164:167], v[50:65]
	s_cmp_ge_i32 s62, s87
	s_cselect_b64 s[8:9], -1, 0
	s_cmp_lt_i32 s62, s88
	s_cselect_b64 s[20:21], -1, 0
	s_and_b64 s[8:9], s[8:9], s[20:21]
	s_sub_i32 s20, s62, s0
	s_mulk_i32 s20, 0x7c
	s_waitcnt lgkmcnt(2)
	v_mfma_f32_32x32x16_bf16 v[50:65], v[140:143], v[168:171], v[50:65]
	s_waitcnt lgkmcnt(0)
	v_mfma_f32_32x32x16_bf16 v[50:65], v[144:147], v[200:203], v[50:65]
	ds_read_b64_tr_b16 v[160:161], v1 offset:512
	ds_read_b64_tr_b16 v[162:163], v1 offset:2560
	ds_read_b64_tr_b16 v[164:165], v1 offset:4608
	ds_read_b64_tr_b16 v[166:167], v1 offset:6656
	ds_read_b64_tr_b16 v[168:169], v1 offset:8704
	ds_read_b64_tr_b16 v[170:171], v1 offset:10752
	ds_read_b64_tr_b16 v[200:201], v1 offset:12800
	ds_read_b64_tr_b16 v[202:203], v1 offset:14848
	s_waitcnt lgkmcnt(6)
	v_mfma_f32_32x32x16_bf16 v[34:49], v[66:69], v[160:163], v[34:49]
	s_waitcnt lgkmcnt(4)
	v_mfma_f32_32x32x16_bf16 v[34:49], v[70:73], v[164:167], v[34:49]
	s_waitcnt lgkmcnt(2)
	v_mfma_f32_32x32x16_bf16 v[34:49], v[140:143], v[168:171], v[34:49]
	s_waitcnt lgkmcnt(0)
	v_mfma_f32_32x32x16_bf16 v[34:49], v[144:147], v[200:203], v[34:49]
	ds_read_b64_tr_b16 v[160:161], v1 offset:1024
	ds_read_b64_tr_b16 v[162:163], v1 offset:3072
	ds_read_b64_tr_b16 v[164:165], v1 offset:5120
	ds_read_b64_tr_b16 v[166:167], v1 offset:7168
	ds_read_b64_tr_b16 v[168:169], v1 offset:9216
	ds_read_b64_tr_b16 v[170:171], v1 offset:11264
	ds_read_b64_tr_b16 v[200:201], v1 offset:13312
	ds_read_b64_tr_b16 v[202:203], v1 offset:15360
	s_waitcnt lgkmcnt(6)
	v_mfma_f32_32x32x16_bf16 v[18:33], v[66:69], v[160:163], v[18:33]
	s_waitcnt lgkmcnt(4)
	v_mfma_f32_32x32x16_bf16 v[18:33], v[70:73], v[164:167], v[18:33]
	s_waitcnt lgkmcnt(2)
	v_mfma_f32_32x32x16_bf16 v[18:33], v[140:143], v[168:171], v[18:33]
	s_waitcnt lgkmcnt(0)
	v_mfma_f32_32x32x16_bf16 v[18:33], v[144:147], v[200:203], v[18:33]
	ds_read_b64_tr_b16 v[160:161], v1 offset:1536
	ds_read_b64_tr_b16 v[162:163], v1 offset:3584
	ds_read_b64_tr_b16 v[164:165], v1 offset:5632
	ds_read_b64_tr_b16 v[166:167], v1 offset:7680
	ds_read_b64_tr_b16 v[168:169], v1 offset:9728
	ds_read_b64_tr_b16 v[170:171], v1 offset:11776
	ds_read_b64_tr_b16 v[200:201], v1 offset:13824
	ds_read_b64_tr_b16 v[202:203], v1 offset:15872
	v_cndmask_b32_e64 v1, 0, v150, s[8:9]
	v_cndmask_b32_e32 v1, -1, v1, vcc
	v_bfe_i32 v74, v1, 0, 1
	s_waitcnt lgkmcnt(6)
	v_mfma_f32_32x32x16_bf16 v[2:17], v[66:69], v[160:163], v[2:17]
	v_add_u32_e32 v66, s20, v196
	v_add_u32_e32 v66, 0x3a0, v66
	v_mov_b32_e32 v67, s47
	s_waitcnt lgkmcnt(4)
	v_mfma_f32_32x32x16_bf16 v[2:17], v[70:73], v[164:167], v[2:17]
	s_waitcnt lgkmcnt(2)
	v_mfma_f32_32x32x16_bf16 v[2:17], v[140:143], v[168:171], v[2:17]
	v_cndmask_b32_e64 v140, 0, v184, s[8:9]
	s_and_b64 s[8:9], vcc, s[8:9]
	v_cndmask_b32_e64 v141, v67, v66, s[8:9]
	ds_read2_b32 v[66:67], v141 offset1:1
	ds_read2_b32 v[68:69], v141 offset0:2 offset1:3
	ds_read2_b32 v[70:71], v141 offset0:8 offset1:9
	ds_read2_b32 v[72:73], v141 offset0:10 offset1:11
	s_waitcnt lgkmcnt(3)
	v_bfi_b32 v66, v74, v66, v175
	v_bfe_i32 v74, v1, 1, 1
	v_mfma_f32_32x32x16_bf16 v[2:17], v[144:147], v[200:203], v[2:17]
	v_bfi_b32 v67, v74, v67, v175
	v_bfe_i32 v74, v1, 2, 1
	s_waitcnt lgkmcnt(2)
	v_bfi_b32 v68, v74, v68, v175
	v_bfe_i32 v74, v1, 3, 1
	v_bfi_b32 v69, v74, v69, v175
	v_bfe_i32 v74, v1, 8, 1
	s_waitcnt lgkmcnt(1)
	v_bfi_b32 v70, v74, v70, v175
	v_bfe_i32 v74, v1, 9, 1
	v_bfi_b32 v71, v74, v71, v175
	v_bfe_i32 v74, v1, 10, 1
	s_waitcnt lgkmcnt(0)
	v_bfi_b32 v72, v74, v72, v175
	v_bfe_i32 v74, v1, 11, 1
	v_bfi_b32 v73, v74, v73, v175
	v_pk_fma_f32 v[66:67], v[92:93], s[28:29], v[66:67] op_sel_hi:[1,0,1]
	v_pk_fma_f32 v[68:69], v[94:95], s[28:29], v[68:69] op_sel_hi:[1,0,1]
	v_pk_fma_f32 v[70:71], v[96:97], s[28:29], v[70:71] op_sel_hi:[1,0,1]
	v_pk_fma_f32 v[72:73], v[98:99], s[28:29], v[72:73] op_sel_hi:[1,0,1]
	ds_read2_b32 v[74:75], v141 offset0:16 offset1:17
	v_bfe_i32 v98, v1, 16, 1
	ds_read2_b32 v[92:93], v141 offset0:18 offset1:19
	ds_read2_b32 v[94:95], v141 offset0:24 offset1:25
	ds_read2_b32 v[96:97], v141 offset0:26 offset1:27
	s_waitcnt lgkmcnt(3)
	v_bfi_b32 v74, v98, v74, v175
	v_bfe_i32 v98, v1, 17, 1
	v_bfi_b32 v75, v98, v75, v175
	v_bfe_i32 v98, v1, 18, 1
	s_waitcnt lgkmcnt(2)
	v_bfi_b32 v92, v98, v92, v175
	v_bfe_i32 v98, v1, 19, 1
	v_bfi_b32 v93, v98, v93, v175
	v_bfe_i32 v98, v1, 24, 1
	s_waitcnt lgkmcnt(1)
	v_bfi_b32 v94, v98, v94, v175
	v_bfe_i32 v98, v1, 25, 1
	v_bfi_b32 v95, v98, v95, v175
	v_bfe_i32 v98, v1, 26, 1
	s_waitcnt lgkmcnt(0)
	v_bfi_b32 v96, v98, v96, v175
	v_bfe_i32 v1, v1, 27, 1
	v_bfi_b32 v97, v1, v97, v175
	v_pk_fma_f32 v[74:75], v[100:101], s[28:29], v[74:75] op_sel_hi:[1,0,1]
	v_pk_fma_f32 v[92:93], v[102:103], s[28:29], v[92:93] op_sel_hi:[1,0,1]
	v_pk_fma_f32 v[94:95], v[104:105], s[28:29], v[94:95] op_sel_hi:[1,0,1]
	v_pk_fma_f32 v[96:97], v[106:107], s[28:29], v[96:97] op_sel_hi:[1,0,1]
	v_cndmask_b32_e32 v1, -1, v140, vcc
	ds_read2_b32 v[98:99], v141 offset0:32 offset1:33
	v_bfe_i32 v106, v1, 0, 1
	ds_read2_b32 v[100:101], v141 offset0:34 offset1:35
	ds_read2_b32 v[102:103], v141 offset0:40 offset1:41
	ds_read2_b32 v[104:105], v141 offset0:42 offset1:43
	s_waitcnt lgkmcnt(3)
	v_bfi_b32 v98, v106, v98, v175
	v_bfe_i32 v106, v1, 1, 1
	v_bfi_b32 v99, v106, v99, v175
	s_nop 0
	v_pk_fma_f32 v[76:77], v[76:77], s[28:29], v[98:99] op_sel_hi:[1,0,1]
	v_bfe_i32 v98, v1, 2, 1
	v_bfe_i32 v99, v1, 3, 1
	s_waitcnt lgkmcnt(2)
	v_bfi_b32 v98, v98, v100, v175
	v_bfi_b32 v99, v99, v101, v175
	s_nop 0
	v_pk_fma_f32 v[78:79], v[78:79], s[28:29], v[98:99] op_sel_hi:[1,0,1]
	v_bfe_i32 v98, v1, 8, 1
	v_bfe_i32 v99, v1, 9, 1
	s_waitcnt lgkmcnt(1)
	v_bfi_b32 v98, v98, v102, v175
	v_bfi_b32 v99, v99, v103, v175
	s_nop 0
	v_pk_fma_f32 v[80:81], v[80:81], s[28:29], v[98:99] op_sel_hi:[1,0,1]
	v_bfe_i32 v98, v1, 10, 1
	v_bfe_i32 v99, v1, 11, 1
	s_waitcnt lgkmcnt(0)
	v_bfi_b32 v98, v98, v104, v175
	v_bfi_b32 v99, v99, v105, v175
	s_nop 0
	v_pk_fma_f32 v[82:83], v[82:83], s[28:29], v[98:99] op_sel_hi:[1,0,1]
	ds_read2_b32 v[98:99], v141 offset0:48 offset1:49
	ds_read2_b32 v[100:101], v141 offset0:50 offset1:51
	ds_read2_b32 v[102:103], v141 offset0:56 offset1:57
	ds_read2_b32 v[104:105], v141 offset0:58 offset1:59
	v_bfe_i32 v106, v1, 16, 1
	s_waitcnt lgkmcnt(3)
	v_bfi_b32 v98, v106, v98, v175
	v_bfe_i32 v106, v1, 17, 1
	v_bfi_b32 v99, v106, v99, v175
	s_nop 0
	v_pk_fma_f32 v[84:85], v[84:85], s[28:29], v[98:99] op_sel_hi:[1,0,1]
	v_bfe_i32 v98, v1, 18, 1
	s_waitcnt lgkmcnt(2)
	v_bfi_b32 v98, v98, v100, v175
	v_bfe_i32 v99, v1, 19, 1
	v_bfi_b32 v99, v99, v101, v175
	s_nop 0
	v_pk_fma_f32 v[86:87], v[86:87], s[28:29], v[98:99] op_sel_hi:[1,0,1]
	v_bfe_i32 v98, v1, 24, 1
	s_waitcnt lgkmcnt(1)
	v_bfi_b32 v98, v98, v102, v175
	v_bfe_i32 v99, v1, 25, 1
	v_bfi_b32 v99, v99, v103, v175
	s_nop 0
	v_pk_fma_f32 v[88:89], v[88:89], s[28:29], v[98:99] op_sel_hi:[1,0,1]
	v_bfe_i32 v98, v1, 26, 1
	s_waitcnt lgkmcnt(0)
	v_bfi_b32 v98, v98, v104, v175
	v_bfe_i32 v1, v1, 27, 1
	v_bfi_b32 v99, v1, v105, v175
	s_nop 0
	v_pk_fma_f32 v[90:91], v[90:91], s[28:29], v[98:99] op_sel_hi:[1,0,1]
	v_max_f32_e32 v1, v66, v67
	v_max3_f32 v1, v1, v68, v69
	v_max3_f32 v1, v1, v70, v71
	v_max3_f32 v1, v1, v72, v73
	v_max3_f32 v1, v1, v74, v75
	v_max3_f32 v1, v1, v92, v93
	v_max3_f32 v1, v1, v94, v95
	v_max3_f32 v1, v1, v96, v97
	v_max3_f32 v1, v1, v76, v77
	v_max3_f32 v1, v1, v78, v79
	v_max3_f32 v1, v1, v80, v81
	v_max3_f32 v1, v1, v82, v83
	v_max3_f32 v1, v1, v84, v85
	v_max3_f32 v1, v1, v86, v87
	v_max3_f32 v1, v1, v88, v89
	v_max3_f32 v1, v1, v90, v91
	v_mov_b32_e32 v98, v1
	s_nop 1
	v_permlane32_swap_b32_e32 v1, v98
	v_max_f32_e32 v1, v1, v98
	v_sub_f32_e32 v98, v1, v198
	v_cmp_ge_f32_e32 vcc, s84, v98
	s_cmp_lg_u64 vcc, exec
	s_cbranch_scc1 .LBB0_1584
	v_mov_b32_e32 v169, v198

.LBB0_1577:
	s_mul_hi_i32 s21, s20, 0x3000
	s_mulk_i32 s20, 0x3000
	s_add_u32 s8, s38, s20
	v_sub_f32_e32 v67, v67, v169
	v_sub_f32_e32 v66, v66, v169
	s_addc_u32 s9, s39, s21
	v_exp_f32_e32 v140, v66
	v_exp_f32_e32 v141, v67
	v_lshl_add_u64 v[66:67], v[154:155], 1, s[8:9]
	s_add_i32 s8, s89, s95
	s_mov_b32 s9, m0
	s_mov_b32 m0, s8
	s_nop 0
	global_load_lds_dwordx4 v[66:67], off
	s_mov_b32 m0, s9
	s_add_i32 s8, s89, s96
	v_lshl_add_u64 v[66:67], v[66:67], 0, s[30:31]
	s_mov_b32 s9, m0
	s_mov_b32 m0, s8
	s_nop 0
	global_load_lds_dwordx4 v[66:67], off
	s_mov_b32 m0, s9
	s_add_u32 s8, s93, s20
	s_addc_u32 s9, s94, s21
	s_or_b32 s20, s89, 0x4000
	v_lshl_add_u64 v[66:67], v[152:153], 1, s[8:9]
	s_add_i32 s21, s20, s95
	s_mov_b32 s62, m0
	s_mov_b32 m0, s21
	s_nop 0
	global_load_lds_dwordx4 v[66:67], off
	s_mov_b32 m0, s62
	v_lshl_add_u64 v[66:67], v[156:157], 1, s[8:9]
	s_add_i32 s20, s20, s96
	s_mov_b32 s8, m0
	s_mov_b32 m0, s20
	s_nop 0
	global_load_lds_dwordx4 v[66:67], off
	s_mov_b32 m0, s8
	v_sub_f32_e32 v1, v97, v169
	v_sub_f32_e32 v96, v96, v169
	v_sub_f32_e32 v95, v95, v169
	v_sub_f32_e32 v94, v94, v169
	v_sub_f32_e32 v93, v93, v169
	v_sub_f32_e32 v92, v92, v169
	v_sub_f32_e32 v75, v75, v169
	v_sub_f32_e32 v74, v74, v169
	v_sub_f32_e32 v73, v73, v169
	v_sub_f32_e32 v72, v72, v169
	v_sub_f32_e32 v71, v71, v169
	v_sub_f32_e32 v70, v70, v169
	v_sub_f32_e32 v69, v69, v169
	v_sub_f32_e32 v68, v68, v169
	v_sub_f32_e32 v106, v91, v169
	v_sub_f32_e32 v107, v90, v169
	v_sub_f32_e32 v168, v89, v169
	v_sub_f32_e32 v171, v88, v169
	v_sub_f32_e32 v207, v87, v169
	v_sub_f32_e32 v206, v86, v169
	v_sub_f32_e32 v205, v85, v169
	v_sub_f32_e32 v204, v84, v169
	v_sub_f32_e32 v203, v83, v169
	v_sub_f32_e32 v202, v82, v169
	v_sub_f32_e32 v201, v81, v169
	v_sub_f32_e32 v200, v80, v169
	v_sub_f32_e32 v199, v79, v169
	v_sub_f32_e32 v198, v78, v169
	v_sub_f32_e32 v173, v77, v169
	v_sub_f32_e32 v172, v76, v169
	v_exp_f32_e32 v142, v68
	v_exp_f32_e32 v143, v69
	v_exp_f32_e32 v144, v70
	v_exp_f32_e32 v145, v71
	v_exp_f32_e32 v146, v72
	v_exp_f32_e32 v147, v73
	v_exp_f32_e32 v160, v74
	v_exp_f32_e32 v161, v75
	v_exp_f32_e32 v162, v92
	v_exp_f32_e32 v163, v93
	v_exp_f32_e32 v164, v94
	v_exp_f32_e32 v165, v95
	v_exp_f32_e32 v166, v96
	v_exp_f32_e32 v167, v1
	v_add_u32_e32 v1, s91, v194
	v_add_u32_e32 v70, v1, v192
	ds_read_b128 v[66:69], v70 offset:16384
	ds_read_b128 v[70:73], v70 offset:24576
	v_add_u32_e32 v102, v1, v193
	ds_read_b128 v[98:101], v102 offset:16384
	ds_read_b128 v[102:105], v102 offset:24576
	v_add_u32_e32 v248, v1, v187
	ds_read_b128 v[240:243], v248 offset:16384
	ds_read_b128 v[244:247], v248 offset:24576
	v_exp_f32_e32 v172, v172
	s_waitcnt lgkmcnt(5)
	v_mfma_f32_32x32x16_bf16 v[82:97], v[66:69], v[136:139], 0
	v_exp_f32_e32 v173, v173
	v_exp_f32_e32 v198, v198
	v_exp_f32_e32 v199, v199
	v_exp_f32_e32 v200, v200
	v_exp_f32_e32 v201, v201
	v_exp_f32_e32 v202, v202
	v_exp_f32_e32 v203, v203
	s_waitcnt lgkmcnt(4)
	v_mfma_f32_32x32x16_bf16 v[66:81], v[70:73], v[136:139], 0
	v_exp_f32_e32 v204, v204
	v_exp_f32_e32 v205, v205
	v_exp_f32_e32 v206, v206
	v_exp_f32_e32 v207, v207
	v_exp_f32_e32 v208, v171
	v_exp_f32_e32 v209, v168
	v_exp_f32_e32 v210, v107
	s_waitcnt lgkmcnt(3)
	v_mfma_f32_32x32x16_bf16 v[82:97], v[98:101], v[132:135], v[82:97]
	v_exp_f32_e32 v211, v106
	s_waitcnt lgkmcnt(2)
	v_mfma_f32_32x32x16_bf16 v[66:81], v[102:105], v[132:135], v[66:81]
	v_add_u32_e32 v102, v1, v186
	ds_read_b128 v[98:101], v102 offset:16384
	ds_read_b128 v[102:105], v102 offset:24576
	s_waitcnt lgkmcnt(3)
	v_mfma_f32_32x32x16_bf16 v[82:97], v[240:243], v[128:131], v[82:97]
	s_waitcnt lgkmcnt(2)
	v_mfma_f32_32x32x16_bf16 v[66:81], v[244:247], v[128:131], v[66:81]
	v_add_u32_e32 v248, v1, v189
	ds_read_b128 v[240:243], v248 offset:16384
	ds_read_b128 v[244:247], v248 offset:24576
	s_waitcnt lgkmcnt(3)
	v_mfma_f32_32x32x16_bf16 v[82:97], v[98:101], v[124:127], v[82:97]
	s_waitcnt lgkmcnt(2)
	v_mfma_f32_32x32x16_bf16 v[66:81], v[102:105], v[124:127], v[66:81]
	v_add_u32_e32 v102, v1, v190
	ds_read_b128 v[98:101], v102 offset:16384
	ds_read_b128 v[102:105], v102 offset:24576
	s_waitcnt lgkmcnt(3)
	v_mfma_f32_32x32x16_bf16 v[82:97], v[240:243], v[120:123], v[82:97]
	s_waitcnt lgkmcnt(2)
	v_mfma_f32_32x32x16_bf16 v[66:81], v[244:247], v[120:123], v[66:81]
	v_add_u32_e32 v248, v1, v185
	ds_read_b128 v[240:243], v248 offset:16384
	ds_read_b128 v[244:247], v248 offset:24576
	s_waitcnt lgkmcnt(3)
	v_mfma_f32_32x32x16_bf16 v[82:97], v[98:101], v[116:119], v[82:97]
	s_waitcnt lgkmcnt(2)
	v_mfma_f32_32x32x16_bf16 v[66:81], v[102:105], v[116:119], v[66:81]
	v_add_u32_e32 v1, v1, v188
	ds_read_b128 v[98:101], v1 offset:16384
	ds_read_b128 v[102:105], v1 offset:24576
	s_waitcnt lgkmcnt(3)
	v_mfma_f32_32x32x16_bf16 v[82:97], v[240:243], v[112:115], v[82:97]
	s_waitcnt lgkmcnt(2)
	v_mfma_f32_32x32x16_bf16 v[66:81], v[244:247], v[112:115], v[66:81]
	s_waitcnt lgkmcnt(1)
	v_mfma_f32_32x32x16_bf16 v[82:97], v[98:101], v[108:111], v[82:97]
	v_add_f32_e64 v98, v140, 0
	v_add_f32_e64 v99, v141, 0
	v_add_f32_e64 v98, v172, v98
	v_add_f32_e64 v99, v173, v99
	v_add_f32_e64 v98, v142, v98
	v_add_f32_e64 v99, v143, v99
	v_pk_add_f32 v[98:99], v[198:199], v[98:99]
	s_waitcnt lgkmcnt(0)
	v_mfma_f32_32x32x16_bf16 v[66:81], v[102:105], v[108:111], v[66:81]
	v_add_f32_e64 v98, v144, v98
	v_add_f32_e64 v99, v145, v99
	v_add_f32_e64 v98, v200, v98
	v_add_f32_e64 v99, v201, v99
	v_add_f32_e64 v98, v146, v98
	v_add_f32_e64 v99, v147, v99
	v_pk_add_f32 v[98:99], v[202:203], v[98:99]
	s_nop 0
	v_pk_add_f32 v[98:99], v[160:161], v[98:99]
	s_nop 0
	v_pk_add_f32 v[98:99], v[204:205], v[98:99]
	s_nop 0
	v_pk_add_f32 v[98:99], v[162:163], v[98:99]
	s_nop 0
	v_pk_add_f32 v[98:99], v[206:207], v[98:99]
	s_nop 0
	v_pk_add_f32 v[98:99], v[164:165], v[98:99]
	s_nop 0
	v_pk_add_f32 v[98:99], v[208:209], v[98:99]
	s_nop 0
	v_pk_add_f32 v[98:99], v[166:167], v[98:99]
	s_nop 0
	v_pk_add_f32 v[98:99], v[210:211], v[98:99]
	s_nop 0
	v_pk_add_f32 v[106:107], v[98:99], v[98:99] op_sel:[0,1] op_sel_hi:[1,0]
	v_cvt_pk_bf16_f32 v98, v140, v141
	v_cvt_pk_bf16_f32 v99, v142, v143
	v_cvt_pk_bf16_f32 v100, v144, v145
	v_cvt_pk_bf16_f32 v101, v146, v147
	v_cvt_pk_bf16_f32 v102, v160, v161
	s_nop 0
	v_mov_b32_e32 v107, v106
	v_cvt_pk_bf16_f32 v103, v162, v163
	v_cvt_pk_bf16_f32 v104, v164, v165
	v_cvt_pk_bf16_f32 v105, v166, v167
	s_nop 1
	v_permlane32_swap_b32_e32 v106, v107
	v_permlane32_swap_b32_e32 v98, v100
	v_permlane32_swap_b32_e32 v99, v101
	v_permlane32_swap_b32_e32 v102, v104
	v_permlane32_swap_b32_e32 v103, v105
	v_cvt_pk_bf16_f32 v140, v172, v173
	v_cvt_pk_bf16_f32 v141, v198, v199
	v_cvt_pk_bf16_f32 v142, v200, v201
	v_cvt_pk_bf16_f32 v143, v202, v203
	v_cvt_pk_bf16_f32 v144, v204, v205
	v_cvt_pk_bf16_f32 v145, v206, v207
	v_cvt_pk_bf16_f32 v146, v208, v209
	v_cvt_pk_bf16_f32 v147, v210, v211
	s_nop 0
	v_permlane32_swap_b32_e32 v140, v142
	v_permlane32_swap_b32_e32 v141, v143
	v_permlane32_swap_b32_e32 v144, v146
	v_permlane32_swap_b32_e32 v145, v147
	v_or_b32_e32 v1, s19, v148
	ds_read_b64_tr_b16 v[160:161], v1
	ds_read_b64_tr_b16 v[162:163], v1 offset:2048
	ds_read_b64_tr_b16 v[164:165], v1 offset:4096
	ds_read_b64_tr_b16 v[166:167], v1 offset:6144
	ds_read_b64_tr_b16 v[198:199], v1 offset:8192
	ds_read_b64_tr_b16 v[200:201], v1 offset:10240
	ds_read_b64_tr_b16 v[202:203], v1 offset:12288
	ds_read_b64_tr_b16 v[204:205], v1 offset:14336
	s_waitcnt lgkmcnt(6)
	v_mfma_f32_32x32x16_bf16 v[50:65], v[98:101], v[160:163], v[50:65]
	ds_read_b64_tr_b16 v[160:161], v1 offset:512
	ds_read_b64_tr_b16 v[162:163], v1 offset:2560
	s_add_i32 s8, s18, -3
	s_cmp_le_i32 s16, s44
	s_cselect_b32 s18, s8, 0xfffffc18
	s_and_b64 s[8:9], s[40:41], exec
	s_cselect_b32 s20, -1, s18
	s_cmp_lg_u32 s20, -1
	s_cselect_b64 vcc, -1, 0
	s_waitcnt lgkmcnt(6)
	v_mfma_f32_32x32x16_bf16 v[50:65], v[102:105], v[164:167], v[50:65]
	ds_read_b64_tr_b16 v[164:165], v1 offset:4608
	ds_read_b64_tr_b16 v[166:167], v1 offset:6656
	s_cmp_ge_i32 s20, s87
	s_cselect_b64 s[8:9], -1, 0
	s_cmp_lt_i32 s20, s88
	s_cselect_b64 s[18:19], -1, 0
	s_and_b64 s[8:9], s[8:9], s[18:19]
	s_sub_i32 s18, s20, s0
	s_mulk_i32 s18, 0x7c
	s_waitcnt lgkmcnt(6)
	v_mfma_f32_32x32x16_bf16 v[50:65], v[140:143], v[198:201], v[50:65]
	ds_read_b64_tr_b16 v[198:199], v1 offset:8704
	ds_read_b64_tr_b16 v[200:201], v1 offset:10752
	s_waitcnt lgkmcnt(6)
	v_mfma_f32_32x32x16_bf16 v[50:65], v[144:147], v[202:205], v[50:65]
	ds_read_b64_tr_b16 v[202:203], v1 offset:12800
	ds_read_b64_tr_b16 v[204:205], v1 offset:14848
	s_waitcnt lgkmcnt(6)
	v_mfma_f32_32x32x16_bf16 v[34:49], v[98:101], v[160:163], v[34:49]
	ds_read_b64_tr_b16 v[160:161], v1 offset:1024
	ds_read_b64_tr_b16 v[162:163], v1 offset:3072
	s_waitcnt lgkmcnt(6)
	v_mfma_f32_32x32x16_bf16 v[34:49], v[102:105], v[164:167], v[34:49]
	ds_read_b64_tr_b16 v[164:165], v1 offset:5120
	ds_read_b64_tr_b16 v[166:167], v1 offset:7168
	s_waitcnt lgkmcnt(6)
	v_mfma_f32_32x32x16_bf16 v[34:49], v[140:143], v[198:201], v[34:49]
	ds_read_b64_tr_b16 v[198:199], v1 offset:9216
	ds_read_b64_tr_b16 v[200:201], v1 offset:11264
	s_waitcnt lgkmcnt(6)
	v_mfma_f32_32x32x16_bf16 v[34:49], v[144:147], v[202:205], v[34:49]
	ds_read_b64_tr_b16 v[202:203], v1 offset:13312
	ds_read_b64_tr_b16 v[204:205], v1 offset:15360
	s_waitcnt lgkmcnt(6)
	v_mfma_f32_32x32x16_bf16 v[18:33], v[98:101], v[160:163], v[18:33]
	ds_read_b64_tr_b16 v[160:161], v1 offset:1536
	ds_read_b64_tr_b16 v[162:163], v1 offset:3584
	s_waitcnt lgkmcnt(6)
	v_mfma_f32_32x32x16_bf16 v[18:33], v[102:105], v[164:167], v[18:33]
	ds_read_b64_tr_b16 v[164:165], v1 offset:5632
	ds_read_b64_tr_b16 v[166:167], v1 offset:7680
	s_waitcnt lgkmcnt(6)
	v_mfma_f32_32x32x16_bf16 v[18:33], v[140:143], v[198:201], v[18:33]
	ds_read_b64_tr_b16 v[198:199], v1 offset:9728
	ds_read_b64_tr_b16 v[200:201], v1 offset:11776
	s_waitcnt lgkmcnt(6)
	v_mfma_f32_32x32x16_bf16 v[18:33], v[144:147], v[202:205], v[18:33]
	ds_read_b64_tr_b16 v[202:203], v1 offset:13824
	ds_read_b64_tr_b16 v[204:205], v1 offset:15872
	v_cndmask_b32_e64 v1, 0, v150, s[8:9]
	v_cndmask_b32_e32 v1, -1, v1, vcc
	s_waitcnt lgkmcnt(6)
	v_mfma_f32_32x32x16_bf16 v[2:17], v[98:101], v[160:163], v[2:17]
	v_add_u32_e32 v98, s18, v196
	v_add_u32_e32 v98, 0x3a0, v98
	v_mov_b32_e32 v99, s47
	s_waitcnt lgkmcnt(4)
	v_mfma_f32_32x32x16_bf16 v[2:17], v[102:105], v[164:167], v[2:17]
	s_waitcnt lgkmcnt(2)
	v_mfma_f32_32x32x16_bf16 v[2:17], v[140:143], v[198:201], v[2:17]
	v_cndmask_b32_e64 v140, 0, v184, s[8:9]
	s_and_b64 s[8:9], vcc, s[8:9]
	v_cndmask_b32_e64 v142, v99, v98, s[8:9]
	ds_read2_b32 v[98:99], v142 offset1:1
	ds_read2_b32 v[100:101], v142 offset0:2 offset1:3
	ds_read2_b32 v[102:103], v142 offset0:8 offset1:9
	ds_read2_b32 v[104:105], v142 offset0:10 offset1:11
	v_bfe_i32 v141, v1, 0, 1
	s_waitcnt lgkmcnt(3)
	v_bfi_b32 v98, v141, v98, v175
	v_bfe_i32 v141, v1, 1, 1
	v_mfma_f32_32x32x16_bf16 v[2:17], v[144:147], v[202:205], v[2:17]
	v_bfi_b32 v99, v141, v99, v175
	v_fma_f32 v82, v82, s28, v98
	v_fma_f32 v83, v83, s28, v99
	v_bfe_i32 v98, v1, 2, 1
	v_bfe_i32 v99, v1, 3, 1
	s_waitcnt lgkmcnt(2)
	v_bfi_b32 v98, v98, v100, v175
	v_bfi_b32 v99, v99, v101, v175
	s_nop 0
	v_pk_fma_f32 v[84:85], v[84:85], s[28:29], v[98:99] op_sel_hi:[1,0,1]
	v_bfe_i32 v98, v1, 8, 1
	v_bfe_i32 v99, v1, 9, 1
	s_waitcnt lgkmcnt(1)
	v_bfi_b32 v98, v98, v102, v175
	v_bfi_b32 v99, v99, v103, v175
	s_nop 0
	v_pk_fma_f32 v[86:87], v[86:87], s[28:29], v[98:99] op_sel_hi:[1,0,1]
	v_bfe_i32 v98, v1, 10, 1
	v_bfe_i32 v99, v1, 11, 1
	s_waitcnt lgkmcnt(0)
	v_bfi_b32 v98, v98, v104, v175
	v_bfi_b32 v99, v99, v105, v175
	s_nop 0
	v_pk_fma_f32 v[88:89], v[88:89], s[28:29], v[98:99] op_sel_hi:[1,0,1]
	ds_read2_b32 v[98:99], v142 offset0:16 offset1:17
	v_bfe_i32 v141, v1, 16, 1
	ds_read2_b32 v[100:101], v142 offset0:18 offset1:19
	ds_read2_b32 v[102:103], v142 offset0:24 offset1:25
	ds_read2_b32 v[104:105], v142 offset0:26 offset1:27
	s_waitcnt lgkmcnt(3)
	v_bfi_b32 v98, v141, v98, v175
	v_bfe_i32 v141, v1, 17, 1
	v_bfi_b32 v99, v141, v99, v175
	s_nop 0
	v_pk_fma_f32 v[98:99], v[90:91], s[28:29], v[98:99] op_sel_hi:[1,0,1]
	v_bfe_i32 v90, v1, 18, 1
	s_waitcnt lgkmcnt(2)
	v_bfi_b32 v90, v90, v100, v175
	v_bfe_i32 v91, v1, 19, 1
	v_bfi_b32 v91, v91, v101, v175
	s_nop 0
	v_pk_fma_f32 v[92:93], v[92:93], s[28:29], v[90:91] op_sel_hi:[1,0,1]
	v_bfe_i32 v90, v1, 24, 1
	s_waitcnt lgkmcnt(1)
	v_bfi_b32 v90, v90, v102, v175
	v_bfe_i32 v91, v1, 25, 1
	v_bfi_b32 v91, v91, v103, v175
	s_nop 0
	v_pk_fma_f32 v[100:101], v[94:95], s[28:29], v[90:91] op_sel_hi:[1,0,1]
	v_bfe_i32 v90, v1, 26, 1
	v_bfe_i32 v1, v1, 27, 1
	s_waitcnt lgkmcnt(0)
	v_bfi_b32 v90, v90, v104, v175
	v_bfi_b32 v91, v1, v105, v175
	v_cndmask_b32_e32 v1, -1, v140, vcc
	v_pk_fma_f32 v[102:103], v[96:97], s[28:29], v[90:91] op_sel_hi:[1,0,1]
	ds_read2_b32 v[90:91], v142 offset0:32 offset1:33
	v_bfe_i32 v140, v1, 0, 1
	ds_read2_b32 v[94:95], v142 offset0:34 offset1:35
	ds_read2_b32 v[96:97], v142 offset0:40 offset1:41
	ds_read2_b32 v[104:105], v142 offset0:42 offset1:43
	s_waitcnt lgkmcnt(3)
	v_bfi_b32 v90, v140, v90, v175
	v_bfe_i32 v140, v1, 1, 1
	v_bfi_b32 v91, v140, v91, v175
	s_nop 0
	v_pk_fma_f32 v[90:91], v[66:67], s[28:29], v[90:91] op_sel_hi:[1,0,1]
	v_bfe_i32 v66, v1, 2, 1
	v_bfe_i32 v67, v1, 3, 1
	s_waitcnt lgkmcnt(2)
	v_bfi_b32 v66, v66, v94, v175
	v_bfi_b32 v67, v67, v95, v175
	s_nop 0
	v_pk_fma_f32 v[94:95], v[68:69], s[28:29], v[66:67] op_sel_hi:[1,0,1]
	v_bfe_i32 v66, v1, 8, 1
	v_bfe_i32 v67, v1, 9, 1
	s_waitcnt lgkmcnt(1)
	v_bfi_b32 v66, v66, v96, v175
	v_bfi_b32 v67, v67, v97, v175
	s_nop 0
	v_pk_fma_f32 v[96:97], v[70:71], s[28:29], v[66:67] op_sel_hi:[1,0,1]
	v_bfe_i32 v66, v1, 10, 1
	v_bfe_i32 v67, v1, 11, 1
	s_waitcnt lgkmcnt(0)
	v_bfi_b32 v66, v66, v104, v175
	v_bfi_b32 v67, v67, v105, v175
	s_nop 0
	v_pk_fma_f32 v[104:105], v[72:73], s[28:29], v[66:67] op_sel_hi:[1,0,1]
	ds_read2_b32 v[66:67], v142 offset0:48 offset1:49
	ds_read2_b32 v[68:69], v142 offset0:50 offset1:51
	ds_read2_b32 v[140:141], v142 offset0:56 offset1:57
	ds_read2_b32 v[142:143], v142 offset0:58 offset1:59
	v_bfe_i32 v70, v1, 16, 1
	s_waitcnt lgkmcnt(3)
	v_bfi_b32 v66, v70, v66, v175
	v_bfe_i32 v70, v1, 17, 1
	v_bfi_b32 v67, v70, v67, v175
	s_nop 0
	v_pk_fma_f32 v[72:73], v[74:75], s[28:29], v[66:67] op_sel_hi:[1,0,1]
	v_bfe_i32 v66, v1, 18, 1
	s_waitcnt lgkmcnt(2)
	v_bfi_b32 v66, v66, v68, v175
	v_bfe_i32 v67, v1, 19, 1
	v_bfi_b32 v67, v67, v69, v175
	s_nop 0
	v_pk_fma_f32 v[70:71], v[76:77], s[28:29], v[66:67] op_sel_hi:[1,0,1]
	v_bfe_i32 v66, v1, 24, 1
	s_waitcnt lgkmcnt(1)
	v_bfi_b32 v66, v66, v140, v175
	v_bfe_i32 v67, v1, 25, 1
	v_bfi_b32 v67, v67, v141, v175
	s_nop 0
	v_pk_fma_f32 v[68:69], v[78:79], s[28:29], v[66:67] op_sel_hi:[1,0,1]
	v_bfe_i32 v66, v1, 26, 1
	s_waitcnt lgkmcnt(0)
	v_bfi_b32 v66, v66, v142, v175
	v_bfe_i32 v1, v1, 27, 1
	v_bfi_b32 v67, v1, v143, v175
	s_nop 0
	v_pk_fma_f32 v[66:67], v[80:81], s[28:29], v[66:67] op_sel_hi:[1,0,1]
	v_max_f32_e32 v1, v82, v83
	v_max3_f32 v1, v1, v84, v85
	v_max3_f32 v1, v1, v86, v87
	v_max3_f32 v1, v1, v88, v89
	v_max3_f32 v1, v1, v98, v99
	v_max3_f32 v1, v1, v92, v93
	v_max3_f32 v1, v1, v100, v101
	v_max3_f32 v1, v1, v102, v103
	v_max3_f32 v1, v1, v90, v91
	v_max3_f32 v1, v1, v94, v95
	v_max3_f32 v1, v1, v96, v97
	v_max3_f32 v1, v1, v104, v105
	v_max3_f32 v1, v1, v72, v73
	v_max3_f32 v1, v1, v70, v71
	v_max3_f32 v1, v1, v68, v69
	v_max3_f32 v1, v1, v66, v67
	v_mov_b32_e32 v74, v1
	s_nop 1
	v_permlane32_swap_b32_e32 v1, v74
	v_max_f32_e32 v1, v1, v74
	v_sub_f32_e32 v74, v1, v159
	v_cmp_ge_f32_e32 vcc, s84, v74
	s_cmp_eq_u64 vcc, exec
	s_cbranch_scc0 .LBB0_1585
	v_mov_b32_e32 v168, 1.0
	v_cmp_gt_f32_e32 vcc, 1.0, v168
	s_cbranch_vccz .LBB0_1582

.LBB0_1587:
	s_add_i32 s6, s90, s97
	s_add_i32 s7, s89, 0
	v_exp_f32_e32 v157, v1
	v_add_u32_e32 v1, s7, v191
	v_add_u32_e32 v82, v1, v192
	v_exp_f32_e32 v156, v80
	v_exp_f32_e32 v152, v78
	v_exp_f32_e32 v153, v79
	ds_read_b128 v[78:81], v82 offset:16384
	v_add_u32_e32 v158, v1, v193
	v_exp_f32_e32 v154, v76
	v_exp_f32_e32 v155, v77
	v_exp_f32_e32 v74, v74
	s_waitcnt lgkmcnt(0)
	v_mfma_f32_32x32x16_bf16 v[92:107], v[78:81], v[136:139], 0
	ds_read_b128 v[76:79], v158 offset:16384
	v_exp_f32_e32 v75, v75
	v_exp_f32_e32 v191, v73
	v_exp_f32_e32 v208, v70
	v_exp_f32_e32 v209, v71
	s_waitcnt lgkmcnt(0)
	v_mfma_f32_32x32x16_bf16 v[92:107], v[76:79], v[132:135], v[92:107]
	ds_read_b128 v[76:79], v82 offset:24576
	s_waitcnt lgkmcnt(0)
	v_mfma_f32_32x32x16_bf16 v[76:91], v[76:79], v[136:139], 0
	ds_read_b128 v[136:139], v158 offset:24576
	v_add_u32_e32 v158, v1, v186
	s_waitcnt lgkmcnt(0)
	v_mfma_f32_32x32x16_bf16 v[76:91], v[136:139], v[132:135], v[76:91]
	v_add_u32_e32 v136, v1, v187
	ds_read_b128 v[132:135], v136 offset:16384
	s_waitcnt lgkmcnt(0)
	v_mfma_f32_32x32x16_bf16 v[92:107], v[132:135], v[128:131], v[92:107]
	ds_read_b128 v[132:135], v136 offset:24576
	ds_read_b128 v[136:139], v158 offset:16384
	ds_read_b128 v[170:173], v158 offset:24576
	v_add_u32_e32 v158, v1, v189
	ds_read_b128 v[192:195], v158 offset:16384
	s_waitcnt lgkmcnt(3)
	v_mfma_f32_32x32x16_bf16 v[76:91], v[132:135], v[128:131], v[76:91]
	ds_read_b128 v[128:131], v158 offset:24576
	v_add_u32_e32 v158, v1, v190
	ds_read_b128 v[132:135], v158 offset:16384
	ds_read_b128 v[196:199], v158 offset:24576
	v_add_u32_e32 v158, v1, v185
	ds_read_b128 v[200:203], v158 offset:16384
	v_add_u32_e32 v1, v1, v188
	s_waitcnt lgkmcnt(6)
	v_mfma_f32_32x32x16_bf16 v[92:107], v[136:139], v[124:127], v[92:107]
	ds_read_b128 v[136:139], v158 offset:24576
	v_exp_f32_e32 v190, v72
	ds_read_b128 v[186:189], v1 offset:16384
	ds_read_b128 v[204:207], v1 offset:24576
	s_waitcnt lgkmcnt(8)
	v_mfma_f32_32x32x16_bf16 v[76:91], v[170:173], v[124:127], v[76:91]
	v_exp_f32_e32 v126, v66
	v_exp_f32_e32 v127, v67
	v_pk_add_f32 v[66:67], v[166:167], 0 op_sel_hi:[1,0]
	v_exp_f32_e32 v124, v68
	v_pk_add_f32 v[66:67], v[66:67], v[156:157]
	v_exp_f32_e32 v125, v69
	v_pk_add_f32 v[66:67], v[164:165], v[66:67]
	s_waitcnt lgkmcnt(7)
	v_mfma_f32_32x32x16_bf16 v[92:107], v[192:195], v[120:123], v[92:107]
	v_add_f32_e64 v66, v152, v66
	v_add_f32_e64 v67, v153, v67
	v_add_f32_e64 v66, v162, v66
	v_add_f32_e64 v67, v163, v67
	v_add_f32_e64 v66, v154, v66
	v_add_f32_e64 v67, v155, v67
	v_pk_add_f32 v[66:67], v[160:161], v[66:67]
	s_waitcnt lgkmcnt(6)
	v_mfma_f32_32x32x16_bf16 v[76:91], v[128:131], v[120:123], v[76:91]
	v_add_f32_e64 v66, v74, v66
	v_add_f32_e64 v67, v75, v67
	v_add_f32_e64 v66, v146, v66
	v_add_f32_e64 v67, v147, v67
	v_add_f32_e64 v66, v190, v66
	v_add_f32_e64 v67, v191, v67
	v_pk_add_f32 v[66:67], v[144:145], v[66:67]
	s_waitcnt lgkmcnt(5)
	v_mfma_f32_32x32x16_bf16 v[92:107], v[132:135], v[116:119], v[92:107]
	v_add_f32_e64 v66, v208, v66
	v_add_f32_e64 v67, v209, v67
	v_add_f32_e64 v66, v142, v66
	v_add_f32_e64 v67, v143, v67
	v_add_f32_e64 v66, v124, v66
	v_add_f32_e64 v67, v125, v67
	v_pk_add_f32 v[66:67], v[140:141], v[66:67]
	s_waitcnt lgkmcnt(4)
	v_mfma_f32_32x32x16_bf16 v[76:91], v[196:199], v[116:119], v[76:91]
	v_add_f32_e64 v66, v126, v66
	v_add_f32_e64 v67, v127, v67
	v_add_f32_e64 v120, v66, v67
	v_add_f32_e64 v121, v67, v66
	v_cvt_pk_bf16_f32 v66, v166, v167
	v_cvt_pk_bf16_f32 v67, v164, v165
	v_cvt_pk_bf16_f32 v68, v162, v163
	v_cvt_pk_bf16_f32 v69, v160, v161
	s_waitcnt lgkmcnt(3)
	v_mfma_f32_32x32x16_bf16 v[92:107], v[200:203], v[112:115], v[92:107]
	v_mov_b32_e32 v1, v120
	v_cvt_pk_bf16_f32 v70, v146, v147
	v_cvt_pk_bf16_f32 v71, v144, v145
	v_cvt_pk_bf16_f32 v72, v142, v143
	v_cvt_pk_bf16_f32 v73, v140, v141
	s_nop 1
	v_permlane32_swap_b32_e32 v120, v1
	s_waitcnt lgkmcnt(2)
	v_mfma_f32_32x32x16_bf16 v[76:91], v[136:139], v[112:115], v[76:91]
	v_permlane32_swap_b32_e32 v66, v68
	v_permlane32_swap_b32_e32 v67, v69
	v_permlane32_swap_b32_e32 v70, v72
	v_permlane32_swap_b32_e32 v71, v73
	s_waitcnt lgkmcnt(1)
	v_mfma_f32_32x32x16_bf16 v[92:107], v[186:189], v[108:111], v[92:107]
	v_cvt_pk_bf16_f32 v116, v156, v157
	v_cvt_pk_bf16_f32 v117, v152, v153
	v_cvt_pk_bf16_f32 v118, v154, v155
	v_cvt_pk_bf16_f32 v119, v74, v75
	v_cvt_pk_bf16_f32 v112, v190, v191
	v_cvt_pk_bf16_f32 v113, v208, v209
	v_cvt_pk_bf16_f32 v114, v124, v125
	s_waitcnt lgkmcnt(0)
	v_mfma_f32_32x32x16_bf16 v[76:91], v[204:207], v[108:111], v[76:91]
	v_cvt_pk_bf16_f32 v115, v126, v127
	v_permlane32_swap_b32_e32 v116, v118
	v_permlane32_swap_b32_e32 v117, v119
	v_permlane32_swap_b32_e32 v112, v114
	v_permlane32_swap_b32_e32 v113, v115
	v_or_b32_e32 v74, s91, v148
	ds_read_b64_tr_b16 v[108:109], v74
	ds_read_b64_tr_b16 v[110:111], v74 offset:2048
	ds_read_b64_tr_b16 v[122:123], v74 offset:4096
	ds_read_b64_tr_b16 v[124:125], v74 offset:6144
	ds_read_b64_tr_b16 v[126:127], v74 offset:8192
	ds_read_b64_tr_b16 v[128:129], v74 offset:10240
	ds_read_b64_tr_b16 v[130:131], v74 offset:12288
	ds_read_b64_tr_b16 v[132:133], v74 offset:14336
	s_waitcnt lgkmcnt(6)
	v_mfma_f32_32x32x16_bf16 v[50:65], v[66:69], v[108:111], v[50:65]
	s_or_b32 s7, s10, 1
	s_add_i32 s6, s6, -4
	s_cmp_le_i32 s7, s10
	s_cselect_b32 s6, s6, 0xfffffc18
	s_cmp_gt_i32 s1, -2
	s_cselect_b32 s1, s6, -1
	s_cmp_lg_u32 s1, -1
	s_waitcnt lgkmcnt(4)
	v_mfma_f32_32x32x16_bf16 v[50:65], v[70:73], v[122:125], v[50:65]
	s_cselect_b64 vcc, -1, 0
	s_cmp_ge_i32 s1, s87
	s_cselect_b64 s[6:7], -1, 0
	s_cmp_lt_i32 s1, s88
	s_cselect_b64 s[8:9], -1, 0
	s_sub_i32 s0, s1, s0
	s_mulk_i32 s0, 0x7c
	s_waitcnt lgkmcnt(2)
	v_mfma_f32_32x32x16_bf16 v[50:65], v[116:119], v[126:129], v[50:65]
	s_and_b64 s[6:7], s[6:7], s[8:9]
	s_add_i32 s0, s0, 0
	s_add_i32 s0, s0, 0x1ea00
	s_waitcnt lgkmcnt(0)
	v_mfma_f32_32x32x16_bf16 v[50:65], v[112:115], v[130:133], v[50:65]
	ds_read_b64_tr_b16 v[108:109], v74 offset:512
	ds_read_b64_tr_b16 v[110:111], v74 offset:2560
	ds_read_b64_tr_b16 v[122:123], v74 offset:4608
	ds_read_b64_tr_b16 v[124:125], v74 offset:6656
	ds_read_b64_tr_b16 v[126:127], v74 offset:8704
	ds_read_b64_tr_b16 v[128:129], v74 offset:10752
	ds_read_b64_tr_b16 v[130:131], v74 offset:12800
	ds_read_b64_tr_b16 v[132:133], v74 offset:14848
	s_waitcnt lgkmcnt(6)
	v_mfma_f32_32x32x16_bf16 v[34:49], v[66:69], v[108:111], v[34:49]
	s_waitcnt lgkmcnt(4)
	v_mfma_f32_32x32x16_bf16 v[34:49], v[70:73], v[122:125], v[34:49]
	s_waitcnt lgkmcnt(2)
	v_mfma_f32_32x32x16_bf16 v[34:49], v[116:119], v[126:129], v[34:49]
	s_waitcnt lgkmcnt(0)
	v_mfma_f32_32x32x16_bf16 v[34:49], v[112:115], v[130:133], v[34:49]
	ds_read_b64_tr_b16 v[108:109], v74 offset:1024
	ds_read_b64_tr_b16 v[110:111], v74 offset:3072
	ds_read_b64_tr_b16 v[122:123], v74 offset:5120
	ds_read_b64_tr_b16 v[124:125], v74 offset:7168
	ds_read_b64_tr_b16 v[126:127], v74 offset:9216
	ds_read_b64_tr_b16 v[128:129], v74 offset:11264
	ds_read_b64_tr_b16 v[130:131], v74 offset:13312
	ds_read_b64_tr_b16 v[132:133], v74 offset:15360
	s_waitcnt lgkmcnt(6)
	v_mfma_f32_32x32x16_bf16 v[18:33], v[66:69], v[108:111], v[18:33]
	s_waitcnt lgkmcnt(4)
	v_mfma_f32_32x32x16_bf16 v[18:33], v[70:73], v[122:125], v[18:33]
	s_waitcnt lgkmcnt(2)
	v_mfma_f32_32x32x16_bf16 v[18:33], v[116:119], v[126:129], v[18:33]
	s_waitcnt lgkmcnt(0)
	v_mfma_f32_32x32x16_bf16 v[18:33], v[112:115], v[130:133], v[18:33]
	ds_read_b64_tr_b16 v[108:109], v74 offset:1536
	ds_read_b64_tr_b16 v[110:111], v74 offset:3584
	ds_read_b64_tr_b16 v[122:123], v74 offset:5632
	ds_read_b64_tr_b16 v[124:125], v74 offset:7680
	ds_read_b64_tr_b16 v[126:127], v74 offset:9728
	ds_read_b64_tr_b16 v[128:129], v74 offset:11776
	ds_read_b64_tr_b16 v[130:131], v74 offset:13824
	ds_read_b64_tr_b16 v[132:133], v74 offset:15872
	s_waitcnt lgkmcnt(6)
	v_mfma_f32_32x32x16_bf16 v[2:17], v[66:69], v[108:111], v[2:17]
	v_cndmask_b32_e64 v66, 0, v150, s[6:7]
	v_cndmask_b32_e32 v108, -1, v66, vcc
	v_lshl_add_u32 v66, v183, 2, s0
	v_cndmask_b32_e64 v109, 0, v184, s[6:7]
	s_and_b64 s[6:7], vcc, s[6:7]
	v_add_u32_e32 v66, 0x3a0, v66
	v_mov_b32_e32 v67, s47
	s_waitcnt lgkmcnt(4)
	v_mfma_f32_32x32x16_bf16 v[2:17], v[70:73], v[122:125], v[2:17]
	v_cndmask_b32_e64 v110, v67, v66, s[6:7]
	ds_read2_b32 v[66:67], v110 offset1:1
	ds_read2_b32 v[68:69], v110 offset0:2 offset1:3
	ds_read2_b32 v[70:71], v110 offset0:8 offset1:9
	ds_read2_b32 v[72:73], v110 offset0:10 offset1:11
	v_bfe_i32 v74, v108, 0, 1
	s_waitcnt lgkmcnt(3)
	v_bfi_b32 v66, v74, v66, v175
	v_bfe_i32 v74, v108, 1, 1
	v_bfi_b32 v67, v74, v67, v175
	v_bfe_i32 v74, v108, 2, 1
	v_mfma_f32_32x32x16_bf16 v[2:17], v[116:119], v[126:129], v[2:17]
	s_waitcnt lgkmcnt(2)
	v_bfi_b32 v68, v74, v68, v175
	v_bfe_i32 v74, v108, 3, 1
	v_bfi_b32 v69, v74, v69, v175
	v_bfe_i32 v74, v108, 8, 1
	s_waitcnt lgkmcnt(1)
	v_bfi_b32 v70, v74, v70, v175
	v_bfe_i32 v74, v108, 9, 1
	v_bfi_b32 v71, v74, v71, v175
	v_mfma_f32_32x32x16_bf16 v[2:17], v[112:115], v[130:133], v[2:17]
	v_bfe_i32 v74, v108, 10, 1
	s_waitcnt lgkmcnt(0)
	v_bfi_b32 v72, v74, v72, v175
	v_bfe_i32 v74, v108, 11, 1
	v_bfi_b32 v73, v74, v73, v175
	v_fma_f32 v66, v92, s28, v66
	v_fma_f32 v67, v93, s28, v67
	v_pk_fma_f32 v[68:69], v[94:95], s[28:29], v[68:69] op_sel_hi:[1,0,1]
	v_pk_fma_f32 v[70:71], v[96:97], s[28:29], v[70:71] op_sel_hi:[1,0,1]
	v_pk_fma_f32 v[72:73], v[98:99], s[28:29], v[72:73] op_sel_hi:[1,0,1]
	ds_read2_b32 v[74:75], v110 offset0:16 offset1:17
	v_bfe_i32 v98, v108, 16, 1
	ds_read2_b32 v[92:93], v110 offset0:18 offset1:19
	ds_read2_b32 v[94:95], v110 offset0:24 offset1:25
	ds_read2_b32 v[96:97], v110 offset0:26 offset1:27
	s_waitcnt lgkmcnt(3)
	v_bfi_b32 v74, v98, v74, v175
	v_bfe_i32 v98, v108, 17, 1
	v_bfi_b32 v75, v98, v75, v175
	v_bfe_i32 v98, v108, 18, 1
	s_waitcnt lgkmcnt(2)
	v_bfi_b32 v92, v98, v92, v175
	v_bfe_i32 v98, v108, 19, 1
	v_bfi_b32 v93, v98, v93, v175
	v_bfe_i32 v98, v108, 24, 1
	s_waitcnt lgkmcnt(1)
	v_bfi_b32 v94, v98, v94, v175
	v_bfe_i32 v98, v108, 25, 1
	v_bfi_b32 v95, v98, v95, v175
	v_bfe_i32 v98, v108, 26, 1
	s_waitcnt lgkmcnt(0)
	v_bfi_b32 v96, v98, v96, v175
	v_bfe_i32 v98, v108, 27, 1
	v_bfi_b32 v97, v98, v97, v175
	v_pk_fma_f32 v[74:75], v[100:101], s[28:29], v[74:75] op_sel_hi:[1,0,1]
	v_pk_fma_f32 v[92:93], v[102:103], s[28:29], v[92:93] op_sel_hi:[1,0,1]
	v_pk_fma_f32 v[94:95], v[104:105], s[28:29], v[94:95] op_sel_hi:[1,0,1]
	v_pk_fma_f32 v[96:97], v[106:107], s[28:29], v[96:97] op_sel_hi:[1,0,1]
	v_cndmask_b32_e32 v106, -1, v109, vcc
	ds_read2_b32 v[98:99], v110 offset0:32 offset1:33
	v_bfe_i32 v107, v106, 0, 1
	ds_read2_b32 v[100:101], v110 offset0:34 offset1:35
	ds_read2_b32 v[102:103], v110 offset0:40 offset1:41
	ds_read2_b32 v[104:105], v110 offset0:42 offset1:43
	s_waitcnt lgkmcnt(3)
	v_bfi_b32 v98, v107, v98, v175
	v_bfe_i32 v107, v106, 1, 1
	v_bfi_b32 v99, v107, v99, v175
	s_nop 0
	v_pk_fma_f32 v[76:77], v[76:77], s[28:29], v[98:99] op_sel_hi:[1,0,1]
	v_bfe_i32 v98, v106, 2, 1
	v_bfe_i32 v99, v106, 3, 1
	s_waitcnt lgkmcnt(2)
	v_bfi_b32 v98, v98, v100, v175
	v_bfi_b32 v99, v99, v101, v175
	s_nop 0
	v_pk_fma_f32 v[78:79], v[78:79], s[28:29], v[98:99] op_sel_hi:[1,0,1]
	v_bfe_i32 v98, v106, 8, 1
	v_bfe_i32 v99, v106, 9, 1
	s_waitcnt lgkmcnt(1)
	v_bfi_b32 v98, v98, v102, v175
	v_bfi_b32 v99, v99, v103, v175
	s_nop 0
	v_pk_fma_f32 v[80:81], v[80:81], s[28:29], v[98:99] op_sel_hi:[1,0,1]
	v_bfe_i32 v98, v106, 10, 1
	v_bfe_i32 v99, v106, 11, 1
	s_waitcnt lgkmcnt(0)
	v_bfi_b32 v98, v98, v104, v175
	v_bfi_b32 v99, v99, v105, v175
	s_nop 0
	v_pk_fma_f32 v[82:83], v[82:83], s[28:29], v[98:99] op_sel_hi:[1,0,1]
	ds_read2_b32 v[98:99], v110 offset0:48 offset1:49
	v_bfe_i32 v107, v106, 16, 1
	ds_read2_b32 v[100:101], v110 offset0:50 offset1:51
	ds_read2_b32 v[102:103], v110 offset0:56 offset1:57
	ds_read2_b32 v[104:105], v110 offset0:58 offset1:59
	s_waitcnt lgkmcnt(3)
	v_bfi_b32 v98, v107, v98, v175
	v_bfe_i32 v107, v106, 17, 1
	v_bfi_b32 v99, v107, v99, v175
	s_nop 0
	v_pk_fma_f32 v[84:85], v[84:85], s[28:29], v[98:99] op_sel_hi:[1,0,1]
	v_bfe_i32 v98, v106, 18, 1
	v_bfe_i32 v99, v106, 19, 1
	s_waitcnt lgkmcnt(2)
	v_bfi_b32 v98, v98, v100, v175
	v_bfi_b32 v99, v99, v101, v175
	s_nop 0
	v_pk_fma_f32 v[86:87], v[86:87], s[28:29], v[98:99] op_sel_hi:[1,0,1]
	v_bfe_i32 v98, v106, 24, 1
	v_bfe_i32 v99, v106, 25, 1
	s_waitcnt lgkmcnt(1)
	v_bfi_b32 v98, v98, v102, v175
	v_bfi_b32 v99, v99, v103, v175
	s_nop 0
	v_pk_fma_f32 v[88:89], v[88:89], s[28:29], v[98:99] op_sel_hi:[1,0,1]
	v_bfe_i32 v98, v106, 26, 1
	v_bfe_i32 v99, v106, 27, 1
	s_waitcnt lgkmcnt(0)
	v_bfi_b32 v98, v98, v104, v175
	v_bfi_b32 v99, v99, v105, v175
	s_nop 0
	v_pk_fma_f32 v[90:91], v[90:91], s[28:29], v[98:99] op_sel_hi:[1,0,1]
	v_max_f32_e32 v98, v66, v67
	v_max3_f32 v98, v98, v68, v69
	v_max3_f32 v98, v98, v70, v71
	v_max3_f32 v98, v98, v72, v73
	v_max3_f32 v98, v98, v74, v75
	v_max3_f32 v98, v98, v92, v93
	v_max3_f32 v98, v98, v94, v95
	v_max3_f32 v98, v98, v96, v97
	v_max3_f32 v98, v98, v76, v77
	v_max3_f32 v98, v98, v78, v79
	v_max3_f32 v98, v98, v80, v81
	v_max3_f32 v98, v98, v82, v83
	v_max3_f32 v98, v98, v84, v85
	v_max3_f32 v98, v98, v86, v87
	v_max3_f32 v98, v98, v88, v89
	v_max3_f32 v98, v98, v90, v91
	v_mov_b32_e32 v99, v98
	s_nop 1
	v_permlane32_swap_b32_e32 v98, v99
	v_max_f32_e32 v98, v98, v99
	v_sub_f32_e32 v99, v98, v159
	v_cmp_ge_f32_e32 vcc, s84, v99
	s_cmp_lg_u64 vcc, exec
	s_cbranch_scc1 .LBB0_1596
